# plus nt on last-use loads in P5 (q/k/v, OST, c_prev, V, qc/kc, mo) and P4 scan c_loc loads so MIX stays cached for the out-projection GEMM
# speedup vs baseline: 1.0423x; 1.0121x over previous
; #define SC_LOAD(cl_, nl_, cb_) do { _Pragma("unroll") for (int i = 0; i < 16; ++i) cl_[i] = *(const u32x4*)(CL + e0 + (size_t)((cb_) + i) * 32768); \
;             _Pragma("unroll") for (int i = 0; i < 16; ++i) nl_[i] = NL[(size_t)(bh * 128 + (cb_) + i) * 128 + dk]; } while (0)
; DI void mlstm_scan(Frame& F) {
;     ...
;     for (int t = F.vcu + F.G * F.wave; t < 512; t += F.G * NWAVES) {
;         const int bh = t >> 6, dk = (t & 63) * 2 + (lane >> 5), dv = (lane & 31) * 8;
;         const float g0 = Gv[bh * 128 + lane], g1 = Gv[bh * 128 + 64 + lane], l0 = MLv[bh * 128 + lane], l1 = MLv[bh * 128 + 64 + lane];
;         const size_t e0 = (size_t)bh * 128 * 32768 + (size_t)dk * 256 + dv;
;         float st[8];
; #pragma unroll
;         for (int e = 0; e < 8; ++e) st[e] = 0.f;
;         float m = 0.f, ns = 0.f;
;         u32x4 cla[16], clb[16]; float nla[16], nlb[16];
;     ...
;         SC_LOAD(cla, nla, 0);
.LBB0_453:
	s_ashr_i32 s0, s26, 6
	s_lshl_b32 s1, s26, 1
	s_and_b32 s1, s1, 0x7e
	s_lshl_b32 s20, s0, 7
	v_or_b32_e32 v18, s1, v222
	v_or_b32_e32 v2, s20, v224
	s_ashr_i32 s1, s0, 31
	v_ashrrev_i32_e32 v3, 31, v2
	s_lshl_b64 s[0:1], s[0:1], 22
	v_lshlrev_b64 v[4:5], 2, v[2:3]
	v_or_b32_e32 v2, 64, v2
	v_lshl_or_b32 v10, v18, 8, s0
	v_ashrrev_i32_e32 v3, 31, v2
	v_mov_b32_e32 v11, s1
	v_or_b32_e32 v10, v10, v130
	v_lshl_add_u64 v[6:7], s[8:9], 0, v[4:5]
	v_lshlrev_b64 v[2:3], 2, v[2:3]
	v_lshl_add_u64 v[4:5], s[10:11], 0, v[4:5]
	v_lshl_add_u64 v[134:135], v[10:11], 1, s[12:13]
	v_lshl_add_u64 v[8:9], s[8:9], 0, v[2:3]
	global_load_dword v223, v[6:7], off
	global_load_dword v225, v[8:9], off
	global_load_dword v226, v[4:5], off
	global_load_dwordx4 v[106:109], v[134:135], off nt
	v_add_co_u32_e32 v4, vcc, s30, v134
	v_lshl_add_u64 v[2:3], s[10:11], 0, v[2:3]
	s_nop 0
	v_addc_co_u32_e32 v5, vcc, 0, v135, vcc
	global_load_dword v227, v[2:3], off
	global_load_dwordx4 v[98:101], v[4:5], off nt
	v_add_co_u32_e32 v2, vcc, s31, v134
	s_or_b32 s4, s20, 1
	s_nop 0
	v_addc_co_u32_e32 v3, vcc, 0, v135, vcc
	v_add_co_u32_e32 v4, vcc, s34, v134
	v_lshlrev_b32_e32 v132, 2, v18
	s_nop 0
	v_addc_co_u32_e32 v5, vcc, 0, v135, vcc
	global_load_dwordx4 v[90:93], v[2:3], off nt
	global_load_dwordx4 v[82:85], v[4:5], off nt
	v_add_co_u32_e32 v2, vcc, s35, v134
	s_ashr_i32 s5, s4, 31
	s_nop 0
	v_addc_co_u32_e32 v3, vcc, 0, v135, vcc
	v_add_co_u32_e32 v4, vcc, s36, v134
	v_lshl_add_u64 v[136:137], s[6:7], 0, v[132:133]
	s_lshl_b64 s[4:5], s[4:5], 9
	v_addc_co_u32_e32 v5, vcc, 0, v135, vcc
	v_lshl_add_u64 v[20:21], v[136:137], 0, s[4:5]
	s_or_b32 s4, s20, 2
	global_load_dwordx4 v[74:77], v[2:3], off nt
	global_load_dwordx4 v[66:69], v[4:5], off nt
	v_add_co_u32_e32 v2, vcc, s37, v134
	s_ashr_i32 s5, s4, 31
	s_nop 0
	v_addc_co_u32_e32 v3, vcc, 0, v135, vcc
	s_lshl_b64 s[4:5], s[4:5], 9
	v_add_co_u32_e32 v4, vcc, s38, v134
	v_lshl_add_u64 v[26:27], v[136:137], 0, s[4:5]
	s_or_b32 s4, s20, 3
	v_addc_co_u32_e32 v5, vcc, 0, v135, vcc
	s_ashr_i32 s5, s4, 31
	global_load_dwordx4 v[58:61], v[2:3], off nt
	global_load_dwordx4 v[50:53], v[4:5], off nt
	v_add_co_u32_e32 v2, vcc, s39, v134
	s_lshl_b64 s[4:5], s[4:5], 9
	s_nop 0
	v_addc_co_u32_e32 v3, vcc, 0, v135, vcc
	v_lshl_add_u64 v[28:29], v[136:137], 0, s[4:5]
	s_or_b32 s4, s20, 4
	v_add_co_u32_e32 v4, vcc, s40, v134
	s_ashr_i32 s5, s4, 31
	s_nop 0
	v_addc_co_u32_e32 v5, vcc, 0, v135, vcc
	s_lshl_b64 s[4:5], s[4:5], 9
	global_load_dwordx4 v[46:49], v[2:3], off nt
	global_load_dwordx4 v[38:41], v[4:5], off nt
	v_add_co_u32_e32 v2, vcc, s41, v134
	s_waitcnt vmcnt(14)
	v_lshl_add_u64 v[34:35], v[136:137], 0, s[4:5]
	s_or_b32 s4, s20, 5
	v_addc_co_u32_e32 v3, vcc, 0, v135, vcc
	s_ashr_i32 s5, s4, 31
	v_add_co_u32_e32 v4, vcc, s42, v134
	s_lshl_b64 s[4:5], s[4:5], 9
	s_nop 0
	v_addc_co_u32_e32 v5, vcc, 0, v135, vcc
	v_lshl_add_u64 v[36:37], v[136:137], 0, s[4:5]
	s_or_b32 s4, s20, 6
	global_load_dwordx4 v[30:33], v[2:3], off nt
	global_load_dwordx4 v[22:25], v[4:5], off nt
	v_add_co_u32_e32 v2, vcc, s43, v134
	s_ashr_i32 s5, s4, 31
	s_nop 0
	v_addc_co_u32_e32 v3, vcc, 0, v135, vcc
	s_lshl_b64 s[4:5], s[4:5], 9
	v_add_co_u32_e32 v4, vcc, s44, v134
	v_lshl_add_u64 v[42:43], v[136:137], 0, s[4:5]
	s_or_b32 s4, s20, 7
	v_addc_co_u32_e32 v5, vcc, 0, v135, vcc
	s_ashr_i32 s5, s4, 31
	global_load_dwordx4 v[14:17], v[2:3], off nt
	global_load_dwordx4 v[10:13], v[4:5], off nt
	v_add_co_u32_e32 v2, vcc, s45, v134
	s_lshl_b64 s[4:5], s[4:5], 9
	s_nop 0
	v_addc_co_u32_e32 v3, vcc, 0, v135, vcc
	s_ashr_i32 s21, s20, 31
	v_lshl_add_u64 v[44:45], v[136:137], 0, s[4:5]
	s_or_b32 s4, s20, 8
	v_add_co_u32_e32 v4, vcc, s46, v134
	s_lshl_b64 s[22:23], s[20:21], 9
	s_ashr_i32 s5, s4, 31
	v_addc_co_u32_e32 v5, vcc, 0, v135, vcc
	v_lshl_add_u64 v[18:19], v[136:137], 0, s[22:23]
	s_lshl_b64 s[4:5], s[4:5], 9
	global_load_dwordx4 v[6:9], v[2:3], off nt
	s_nop 0
	global_load_dwordx4 v[2:5], v[4:5], off nt
	s_nop 0
	global_load_dword v138, v[18:19], off
	global_load_dword v201, v[20:21], off
	global_load_dword v197, v[26:27], off
	global_load_dword v193, v[28:29], off
	global_load_dword v189, v[34:35], off
	global_load_dword v185, v[36:37], off
	global_load_dword v181, v[42:43], off
	global_load_dword v175, v[44:45], off
	v_lshl_add_u64 v[18:19], v[136:137], 0, s[4:5]
	s_or_b32 s4, s20, 9
	s_ashr_i32 s5, s4, 31
	s_lshl_b64 s[4:5], s[4:5], 9
	v_lshl_add_u64 v[20:21], v[136:137], 0, s[4:5]
	s_or_b32 s4, s20, 10
	s_ashr_i32 s5, s4, 31
	s_lshl_b64 s[4:5], s[4:5], 9
	v_lshl_add_u64 v[26:27], v[136:137], 0, s[4:5]
	s_or_b32 s4, s20, 11
	s_ashr_i32 s5, s4, 31
	s_lshl_b64 s[4:5], s[4:5], 9
	v_lshl_add_u64 v[28:29], v[136:137], 0, s[4:5]
	s_or_b32 s4, s20, 12
	s_ashr_i32 s5, s4, 31
	s_lshl_b64 s[4:5], s[4:5], 9
	v_lshl_add_u64 v[34:35], v[136:137], 0, s[4:5]
	s_or_b32 s4, s20, 13
	s_ashr_i32 s5, s4, 31
	s_lshl_b64 s[4:5], s[4:5], 9
	v_lshl_add_u64 v[36:37], v[136:137], 0, s[4:5]
	s_or_b32 s4, s20, 14
	s_ashr_i32 s5, s4, 31
	s_lshl_b64 s[4:5], s[4:5], 9
	v_lshl_add_u64 v[42:43], v[136:137], 0, s[4:5]
	s_or_b32 s4, s20, 15
	s_ashr_i32 s5, s4, 31
	s_lshl_b64 s[4:5], s[4:5], 9
	v_lshl_add_u64 v[44:45], v[136:137], 0, s[4:5]
	global_load_dword v179, v[18:19], off
	global_load_dword v173, v[20:21], off
	global_load_dword v169, v[26:27], off
	global_load_dword v165, v[28:29], off
	global_load_dword v161, v[34:35], off
	global_load_dword v157, v[36:37], off
	global_load_dword v153, v[42:43], off
	global_load_dword v147, v[44:45], off
	s_and_b32 s4, s28, 0x7e
	v_or_b32_e32 v18, s4, v222
	v_bitop3_b32 v19, s26, 63, v0 bitop3:0xc8
	v_or_b32_e32 v20, s0, v130
	v_cmp_eq_u32_e64 s[4:5], 0, v19
	v_lshl_or_b32 v140, v18, 2, s22
	v_mov_b32_e32 v19, s1
	v_lshl_or_b32 v18, v18, 8, v20
	v_mov_b32_e32 v141, s23
	s_lshl_b64 s[22:23], s[20:21], 2
	v_lshlrev_b64 v[142:143], 1, v[18:19]
	v_mov_b32_e32 v146, 0
	s_mov_b32 s21, s15
	v_mov_b32_e32 v210, 0
	v_mov_b32_e32 v211, v133
	v_mov_b32_e32 v212, 0
	v_mov_b32_e32 v213, v133
	v_mov_b32_e32 v214, 0
	v_mov_b32_e32 v215, v133
	v_mov_b32_e32 v216, 0
	v_mov_b32_e32 v217, v133
	v_mov_b32_e32 v139, v133
	s_branch .LBB0_455

; #define SC_LOAD(cl_, nl_, cb_) do { _Pragma("unroll") for (int i = 0; i < 16; ++i) cl_[i] = *(const u32x4*)(CL + e0 + (size_t)((cb_) + i) * 32768); \
;             _Pragma("unroll") for (int i = 0; i < 16; ++i) nl_[i] = NL[(size_t)(bh * 128 + (cb_) + i) * 128 + dk]; } while (0)
; DI void mlstm_scan(Frame& F) {
;     ...
;         SC_LOAD(cla, nla, 0);
; #pragma unroll 1
;         for (int cb = 0; cb < NCH; cb += 32) {
;             SC_LOAD(clb, nlb, cb + 16);
;             __builtin_amdgcn_sched_barrier(0);
;             SC_BATCH(cla, nla, cb);
;             { const int cn = cb + 32 < NCH ? cb + 32 : cb; SC_LOAD(cla, nla, cn); }
;             __builtin_amdgcn_sched_barrier(0);
;             SC_BATCH(clb, nlb, cb + 16);
.LBB0_455:
	v_lshl_add_u64 v[144:145], s[94:95], 0, v[142:143]
	v_add_co_u32_e32 v18, vcc, s47, v144
	v_lshl_add_u64 v[148:149], s[94:95], 0, v[140:141]
	s_nop 0
	v_addc_co_u32_e32 v19, vcc, 0, v145, vcc
	v_add_co_u32_e32 v20, vcc, s48, v144
	s_nop 1
	v_addc_co_u32_e32 v21, vcc, 0, v145, vcc
	global_load_dwordx4 v[126:129], v[18:19], off nt
	global_load_dwordx4 v[122:125], v[20:21], off nt
	v_add_co_u32_e32 v18, vcc, s49, v144
	s_nop 1
	v_addc_co_u32_e32 v19, vcc, 0, v145, vcc
	v_add_co_u32_e32 v20, vcc, s50, v144
	s_nop 1
	v_addc_co_u32_e32 v21, vcc, 0, v145, vcc
	global_load_dwordx4 v[118:121], v[18:19], off nt
	global_load_dwordx4 v[114:117], v[20:21], off nt
	v_add_co_u32_e32 v18, vcc, s51, v144
	s_nop 1
	v_addc_co_u32_e32 v19, vcc, 0, v145, vcc
	v_add_co_u32_e32 v20, vcc, s52, v144
	s_nop 1
	v_addc_co_u32_e32 v21, vcc, 0, v145, vcc
	global_load_dwordx4 v[110:113], v[18:19], off nt
	global_load_dwordx4 v[102:105], v[20:21], off nt
	v_add_co_u32_e32 v18, vcc, s53, v144
	s_nop 1
	v_addc_co_u32_e32 v19, vcc, 0, v145, vcc
	v_add_co_u32_e32 v20, vcc, s54, v144
	s_nop 1
	v_addc_co_u32_e32 v21, vcc, 0, v145, vcc
	global_load_dwordx4 v[94:97], v[18:19], off nt
	global_load_dwordx4 v[86:89], v[20:21], off nt
	v_add_co_u32_e32 v18, vcc, s55, v144
	s_nop 1
	v_addc_co_u32_e32 v19, vcc, 0, v145, vcc
	v_add_co_u32_e32 v20, vcc, s56, v144
	s_nop 1
	v_addc_co_u32_e32 v21, vcc, 0, v145, vcc
	global_load_dwordx4 v[78:81], v[18:19], off nt
	global_load_dwordx4 v[70:73], v[20:21], off nt
	v_add_co_u32_e32 v18, vcc, s57, v144
	s_nop 1
	v_addc_co_u32_e32 v19, vcc, 0, v145, vcc
	v_add_co_u32_e32 v20, vcc, s58, v144
	s_nop 1
	v_addc_co_u32_e32 v21, vcc, 0, v145, vcc
	global_load_dwordx4 v[62:65], v[18:19], off nt
	global_load_dwordx4 v[54:57], v[20:21], off nt
	v_add_co_u32_e32 v18, vcc, s59, v144
	s_nop 1
	v_addc_co_u32_e32 v19, vcc, 0, v145, vcc
	v_add_co_u32_e32 v20, vcc, s60, v144
	s_nop 1
	v_addc_co_u32_e32 v21, vcc, 0, v145, vcc
	global_load_dwordx4 v[42:45], v[18:19], off nt
	global_load_dwordx4 v[34:37], v[20:21], off nt
	v_add_co_u32_e32 v18, vcc, s61, v144
	s_nop 1
	v_addc_co_u32_e32 v19, vcc, 0, v145, vcc
	v_add_co_u32_e32 v20, vcc, s62, v144
	s_nop 1
	v_addc_co_u32_e32 v21, vcc, 0, v145, vcc
	v_add_co_u32_e32 v150, vcc, s63, v148
	global_load_dwordx4 v[26:29], v[18:19], off nt
	s_nop 0
	global_load_dwordx4 v[18:21], v[20:21], off nt
	v_addc_co_u32_e32 v151, vcc, 0, v149, vcc
	v_add_co_u32_e32 v218, vcc, s64, v148
	s_nop 1
	v_addc_co_u32_e32 v219, vcc, 0, v149, vcc
	global_load_dword v209, v[218:219], off offset:-4096
	global_load_dword v207, v[150:151], off offset:512
	global_load_dword v205, v[150:151], off offset:1024
	global_load_dword v203, v[150:151], off offset:1536
	global_load_dword v199, v[150:151], off offset:2048
	global_load_dword v195, v[150:151], off offset:2560
	global_load_dword v191, v[150:151], off offset:3072
	global_load_dword v187, v[150:151], off offset:3584
	global_load_dword v183, v[218:219], off
	global_load_dword v177, v[218:219], off offset:512
	global_load_dword v171, v[218:219], off offset:1024
	global_load_dword v167, v[218:219], off offset:1536
	global_load_dword v163, v[218:219], off offset:2048
	global_load_dword v159, v[218:219], off offset:2560
	global_load_dword v155, v[218:219], off offset:3072
	global_load_dword v151, v[218:219], off offset:3584
	s_cmp_lt_u32 s21, 64
	s_cselect_b64 vcc, -1, 0
	s_waitcnt vmcnt(62)
	v_cndmask_b32_e32 v150, v225, v223, vcc
	v_cndmask_b32_e32 v228, v227, v226, vcc
	v_readlane_b32 s0, v150, s21
	v_readlane_b32 s1, v228, s21
	v_add_co_u32_e32 v220, vcc, 0x60000000, v144
	v_add_f32_e32 v132, s0, v146
	v_max_f32_e64 v152, s1, s1
	v_max_f32_e32 v152, v132, v152
	v_sub_f32_e32 v132, v132, v152
	v_sub_f32_e32 v154, s1, v152
	v_mul_f32_e32 v132, 0x3fb8aa3b, v132
	v_mul_f32_e32 v154, 0x3fb8aa3b, v154
	v_exp_f32_e32 v132, v132
	v_exp_f32_e32 v218, v154
	v_cvt_pk_bf16_f32 v230, v212, v213
	v_cvt_pk_bf16_f32 v231, v214, v215
	v_cvt_pk_bf16_f32 v232, v216, v217
	v_cvt_pk_bf16_f32 v233, v210, v211
	v_addc_co_u32_e32 v221, vcc, 0, v145, vcc
	global_store_dwordx4 v[220:221], v[230:233], off
	s_and_saveexec_b64 s[0:1], s[2:3]
	s_cbranch_execz .LBB0_457
	v_mov_b32_e32 v219, v132
	s_waitcnt vmcnt(48)
	v_pk_mul_f32 v[220:221], v[138:139], v[218:219]
	s_nop 0
	v_add_f32_e32 v138, v221, v220
	v_add_co_u32_e32 v220, vcc, 0x2480000, v148
	s_nop 1
	v_addc_co_u32_e32 v221, vcc, 0, v149, vcc
	global_store_dword v[220:221], v139, off
	v_mov_b32_e32 v139, v138

; #define SC_LOAD(cl_, nl_, cb_) do { _Pragma("unroll") for (int i = 0; i < 16; ++i) cl_[i] = *(const u32x4*)(CL + e0 + (size_t)((cb_) + i) * 32768); \
;             _Pragma("unroll") for (int i = 0; i < 16; ++i) nl_[i] = NL[(size_t)(bh * 128 + (cb_) + i) * 128 + dk]; } while (0)
; DI void mlstm_scan(Frame& F) {
;     ...
;         SC_LOAD(cla, nla, 0);
; #pragma unroll 1
;         for (int cb = 0; cb < NCH; cb += 32) {
;             SC_LOAD(clb, nlb, cb + 16);
;             __builtin_amdgcn_sched_barrier(0);
;             SC_BATCH(cla, nla, cb);
;             { const int cn = cb + 32 < NCH ? cb + 32 : cb; SC_LOAD(cla, nla, cn); }
;             __builtin_amdgcn_sched_barrier(0);
;             SC_BATCH(clb, nlb, cb + 16);
.LBB0_519:
	s_or_b64 exec, exec, s[0:1]
	s_add_i32 s33, s21, 32
	s_cmpk_gt_u32 s21, 0x5f
	s_cselect_b64 s[24:25], -1, 0
	s_cmpk_lt_u32 s21, 0x60
	s_cselect_b32 s0, s33, s21
	s_lshl_b32 s14, s0, 16
	v_lshlrev_b32_e32 v218, 16, v2
	v_and_b32_e32 v219, 0xffff0000, v2
	v_lshlrev_b32_e32 v230, 16, v3
	v_and_b32_e32 v231, 0xffff0000, v3
	v_lshl_add_u64 v[2:3], v[134:135], 0, s[14:15]
	v_lshlrev_b32_e32 v232, 16, v4
	v_and_b32_e32 v233, 0xffff0000, v4
	v_add_co_u32_e32 v4, vcc, s30, v2
	v_lshlrev_b32_e32 v234, 16, v5
	v_and_b32_e32 v235, 0xffff0000, v5
	v_addc_co_u32_e32 v5, vcc, 0, v3, vcc
	global_load_dwordx4 v[106:109], v[2:3], off nt
	global_load_dwordx4 v[98:101], v[4:5], off nt
	v_add_co_u32_e32 v4, vcc, s31, v2
	s_add_i32 s0, s0, s20
	s_nop 0
	v_addc_co_u32_e32 v5, vcc, 0, v3, vcc
	v_add_co_u32_e32 v6, vcc, s34, v2
	s_ashr_i32 s1, s0, 31
	s_nop 0
	v_addc_co_u32_e32 v7, vcc, 0, v3, vcc
	s_lshl_b64 s[66:67], s[0:1], 9
	global_load_dwordx4 v[90:93], v[4:5], off nt
	global_load_dwordx4 v[82:85], v[6:7], off nt
	v_add_co_u32_e32 v4, vcc, s35, v2
	s_waitcnt vmcnt(52)
	v_lshl_add_u64 v[146:147], v[136:137], 0, s[66:67]
	s_or_b32 s66, s0, 1
	v_addc_co_u32_e32 v5, vcc, 0, v3, vcc
	s_ashr_i32 s67, s66, 31
	v_add_co_u32_e32 v6, vcc, s36, v2
	s_lshl_b64 s[66:67], s[66:67], 9
	s_nop 0
	v_addc_co_u32_e32 v7, vcc, 0, v3, vcc
	v_lshl_add_u64 v[156:157], v[136:137], 0, s[66:67]
	s_or_b32 s66, s0, 2
	global_load_dwordx4 v[74:77], v[4:5], off nt
	global_load_dwordx4 v[66:69], v[6:7], off nt
	v_add_co_u32_e32 v4, vcc, s37, v2
	s_ashr_i32 s67, s66, 31
	s_nop 0
	v_addc_co_u32_e32 v5, vcc, 0, v3, vcc
	s_lshl_b64 s[66:67], s[66:67], 9
	v_add_co_u32_e32 v6, vcc, s38, v2
	v_lshl_add_u64 v[160:161], v[136:137], 0, s[66:67]
	s_or_b32 s66, s0, 3
	v_addc_co_u32_e32 v7, vcc, 0, v3, vcc
	s_ashr_i32 s67, s66, 31
	global_load_dwordx4 v[58:61], v[4:5], off nt
	global_load_dwordx4 v[50:53], v[6:7], off nt
	v_add_co_u32_e32 v4, vcc, s39, v2
	s_lshl_b64 s[66:67], s[66:67], 9
	s_nop 0
	v_addc_co_u32_e32 v5, vcc, 0, v3, vcc
	v_lshl_add_u64 v[164:165], v[136:137], 0, s[66:67]
	s_or_b32 s66, s0, 4
	v_add_co_u32_e32 v6, vcc, s40, v2
	s_ashr_i32 s67, s66, 31
	s_nop 0
	v_addc_co_u32_e32 v7, vcc, 0, v3, vcc
	s_lshl_b64 s[66:67], s[66:67], 9
	global_load_dwordx4 v[46:49], v[4:5], off nt
	global_load_dwordx4 v[38:41], v[6:7], off nt
	v_add_co_u32_e32 v4, vcc, s41, v2
	v_lshl_add_u64 v[168:169], v[136:137], 0, s[66:67]
	s_or_b32 s66, s0, 5
	v_addc_co_u32_e32 v5, vcc, 0, v3, vcc
	s_ashr_i32 s67, s66, 31
	v_add_co_u32_e32 v6, vcc, s42, v2
	s_lshl_b64 s[66:67], s[66:67], 9
	s_nop 0
	v_addc_co_u32_e32 v7, vcc, 0, v3, vcc
	v_lshl_add_u64 v[172:173], v[136:137], 0, s[66:67]
	s_or_b32 s66, s0, 6
	global_load_dwordx4 v[30:33], v[4:5], off nt
	global_load_dwordx4 v[22:25], v[6:7], off nt
	v_add_co_u32_e32 v4, vcc, s43, v2
	s_ashr_i32 s67, s66, 31
	s_nop 0
	v_addc_co_u32_e32 v5, vcc, 0, v3, vcc
	s_lshl_b64 s[66:67], s[66:67], 9
	v_add_co_u32_e32 v6, vcc, s44, v2
	v_lshl_add_u64 v[174:175], v[136:137], 0, s[66:67]
	s_or_b32 s66, s0, 7
	v_addc_co_u32_e32 v7, vcc, 0, v3, vcc
	s_ashr_i32 s67, s66, 31
	global_load_dwordx4 v[14:17], v[4:5], off nt
	global_load_dwordx4 v[10:13], v[6:7], off nt
	v_add_co_u32_e32 v4, vcc, s45, v2
	s_lshl_b64 s[66:67], s[66:67], 9
	s_nop 0
	v_addc_co_u32_e32 v5, vcc, 0, v3, vcc
	v_lshl_add_u64 v[178:179], v[136:137], 0, s[66:67]
	s_or_b32 s66, s0, 8
	v_add_co_u32_e32 v2, vcc, s46, v2
	s_ashr_i32 s67, s66, 31
	s_nop 0
	v_addc_co_u32_e32 v3, vcc, 0, v3, vcc
	s_lshl_b64 s[66:67], s[66:67], 9
	global_load_dwordx4 v[6:9], v[4:5], off nt
	s_nop 0
	global_load_dwordx4 v[2:5], v[2:3], off nt
	s_nop 0
	global_load_dword v138, v[146:147], off
	global_load_dword v201, v[156:157], off
	global_load_dword v197, v[160:161], off
	global_load_dword v193, v[164:165], off
	global_load_dword v189, v[168:169], off
	global_load_dword v185, v[172:173], off
	global_load_dword v181, v[174:175], off
	s_nop 0
	global_load_dword v175, v[178:179], off
	v_lshl_add_u64 v[146:147], v[136:137], 0, s[66:67]
	s_or_b32 s66, s0, 9
	s_ashr_i32 s67, s66, 31
	s_lshl_b64 s[66:67], s[66:67], 9
	v_lshl_add_u64 v[156:157], v[136:137], 0, s[66:67]
	s_or_b32 s66, s0, 10
	s_ashr_i32 s67, s66, 31
	s_lshl_b64 s[66:67], s[66:67], 9
	v_lshl_add_u64 v[160:161], v[136:137], 0, s[66:67]
	s_or_b32 s66, s0, 11
	s_ashr_i32 s67, s66, 31
	s_lshl_b64 s[66:67], s[66:67], 9
	v_lshl_add_u64 v[164:165], v[136:137], 0, s[66:67]
	s_or_b32 s66, s0, 12
	s_ashr_i32 s67, s66, 31
	s_lshl_b64 s[66:67], s[66:67], 9
	v_lshl_add_u64 v[220:221], v[136:137], 0, s[66:67]
	s_or_b32 s66, s0, 13
	s_ashr_i32 s67, s66, 31
	s_lshl_b64 s[66:67], s[66:67], 9
	v_lshl_add_u64 v[236:237], v[136:137], 0, s[66:67]
	s_or_b32 s66, s0, 14
	s_or_b32 s0, s0, 15
	s_ashr_i32 s67, s66, 31
	s_ashr_i32 s1, s0, 31
	s_lshl_b64 s[66:67], s[66:67], 9
	s_lshl_b64 s[0:1], s[0:1], 9
	v_lshl_add_u64 v[238:239], v[136:137], 0, s[66:67]
	v_lshl_add_u64 v[240:241], v[136:137], 0, s[0:1]
	global_load_dword v179, v[146:147], off
	global_load_dword v173, v[156:157], off
	global_load_dword v169, v[160:161], off
	s_nop 0
	global_load_dword v165, v[164:165], off
	s_nop 0
	global_load_dword v161, v[220:221], off
	global_load_dword v157, v[236:237], off
	global_load_dword v153, v[238:239], off
	global_load_dword v147, v[240:241], off
	s_waitcnt vmcnt(1)
	v_pk_mul_f32 v[210:211], v[210:211], v[152:153] op_sel_hi:[1,0]
	s_nop 0
	v_pk_fma_f32 v[220:221], v[132:133], v[218:219], v[210:211] op_sel_hi:[0,1,1]
	v_pk_mul_f32 v[210:211], v[212:213], v[152:153] op_sel_hi:[1,0]
	s_nop 0
	v_pk_fma_f32 v[218:219], v[132:133], v[230:231], v[210:211] op_sel_hi:[0,1,1]
	v_pk_mul_f32 v[210:211], v[214:215], v[152:153] op_sel_hi:[1,0]
	s_nop 0
	v_pk_fma_f32 v[212:213], v[132:133], v[232:233], v[210:211] op_sel_hi:[0,1,1]
	v_pk_mul_f32 v[210:211], v[216:217], v[152:153] op_sel_hi:[1,0]
	s_nop 0
	v_pk_fma_f32 v[210:211], v[132:133], v[234:235], v[210:211] op_sel_hi:[0,1,1]
	s_add_i32 s0, s21, 16
	v_readlane_b32 s1, v150, s0
	v_readlane_b32 s0, v228, s0
	v_add_co_u32_e32 v214, vcc, 0x60100000, v144
	v_add_f32_e32 v132, s1, v154
	v_max_f32_e64 v146, s0, s0
	v_max_f32_e32 v146, v132, v146
	v_sub_f32_e32 v132, v132, v146
	v_mul_f32_e32 v132, 0x3fb8aa3b, v132
	v_exp_f32_e32 v216, v132
	v_sub_f32_e32 v132, s0, v146
	v_mul_f32_e32 v132, 0x3fb8aa3b, v132
	v_exp_f32_e32 v132, v132
	v_cvt_pk_bf16_f32 v230, v220, v221
	v_cvt_pk_bf16_f32 v231, v218, v219
	v_cvt_pk_bf16_f32 v232, v212, v213
	v_cvt_pk_bf16_f32 v233, v210, v211
	v_addc_co_u32_e32 v215, vcc, 0, v145, vcc
	global_store_dwordx4 v[214:215], v[230:233], off
	s_and_saveexec_b64 s[0:1], s[2:3]
	s_cbranch_execz .LBB0_521
	v_mov_b32_e32 v208, v139
	v_mov_b32_e32 v217, v132
	v_pk_mul_f32 v[208:209], v[208:209], v[216:217]
	s_nop 0
	v_add_f32_e32 v152, v208, v209
	v_add_co_u32_e32 v208, vcc, 0x2482000, v148
	s_nop 1
	v_addc_co_u32_e32 v209, vcc, 0, v149, vcc
	global_store_dword v[208:209], v139, off
	v_mov_b32_e32 v139, v152

; DI float log_sigmoid(float x) { return fminf(x, 0.f) - log1pf(__expf(-fabsf(x))); }
; DI void mlstm_m3_unit(Frame& F, int u) {
;     ...
;     const bf16* CP = (const bf16*)(F.ws + WS_CPREV) + (size_t)u * 32768;
;     dma_img128(imgV0, PROJ + (size_t)tok0 * NPROJ + COL_MV + hd * 256, NPROJ, F.wave, lane);
;     dma_img128(imgV1, PROJ + (size_t)tok0 * NPROJ + COL_MV + hd * 256 + 128, NPROJ, F.wave, lane);
;     dma_img128(imgC0, CP, 256, F.wave, lane);
;     dma_img128(imgC1, CP + 128, 256, F.wave, lane);
;     asm volatile("" ::: "memory");
;     const int tb = F.wave & 3, dh = F.wave >> 2;
;     const int tl = 32 * tb + r;
;     bf16x8 qf[8];
;     { const bf16* qp = QC + (size_t)(tok0 + tl) * 512 + hd * 128 + 8 * h;
; #pragma unroll
;       for (int kk = 0; kk < 8; ++kk) qf[kk] = *(const bf16x8*)(qp + 16 * kk); }
;     u32x4 kreg[4];
; #pragma unroll
;     for (int it = 0; it < 4; ++it) { const int idx = tid_ + NTHR * it, row = idx >> 4, ch = idx & 15; kreg[it] = *(const u32x4*)(KC + (size_t)(tok0 + row) * 512 + hd * 128 + 8 * ch); }
;     asm volatile("" ::: "memory");
;     const float m_prev = ((const float*)(F.ws + WS_SMALL + SM_MPREV))[u];
;     if (F.wave == 0) {
;         const int s0 = 2 * lane;
;         const float ig0 = GATES[(size_t)(tok0 + s0) * 8 + hd], fg0 = GATES[(size_t)(tok0 + s0) * 8 + 4 + hd];
;         const float ig1 = GATES[(size_t)(tok0 + s0 + 1) * 8 + hd], fg1 = GATES[(size_t)(tok0 + s0 + 1) * 8 + 4 + hd];
;         const float lf0 = log_sigmoid(fg0), lf1 = log_sigmoid(fg1);
;         const float b1 = scan_incl_sum(lf0 + lf1, lane), b0 = b1 - lf1;
;         const float u0 = ig0 - b0, u1 = ig1 - b1;
;         const float im = scan_incl_max(fmaxf(u0, u1), lane);
;         float ex = __shfl_up(im, 1); if (lane == 0) ex = -1e30f;
;         const float cm0 = fmaxf(ex, u0), cm1 = im;
;         const float M0 = fmaxf(m_prev, cm0), M1 = fmaxf(m_prev, cm1);
;         mf[s0] = u0; mf[s0 + 1] = u1; mf[128 + s0] = M0; mf[128 + s0 + 1] = M1;
;         mf[256 + s0] = __expf(m_prev - M0); mf[256 + s0 + 1] = __expf(m_prev - M1);
;         mf[384 + s0] = __expf(-(b0 + M0)); mf[384 + s0 + 1] = __expf(-(b1 + M1));
;     }
;     if (F.wave == 1) { const float* NP = (const float*)(F.ws + WS_SMALL + SM_NPREV) + (size_t)u * 128; mf[512 + lane] = NP[lane]; mf[512 + 64 + lane] = NP[64 + lane]; }
.LBB0_678:
	s_lshl_b32 s0, s36, 5
	s_lshl_b32 s1, s36, 7
	s_and_b32 s0, s0, 0xffffc000
	s_and_b32 s1, s1, 0x3f80
	s_ashr_i32 s37, s36, 31
	s_bfe_u32 s2, s36, 0x20007
	s_or_b32 s3, s0, s1
	s_lshl_b64 s[0:1], s[36:37], 16
	s_add_u32 s0, s38, s0
	s_addc_u32 s1, s39, s1
	s_mul_i32 s5, s3, 0x3000
	s_mul_hi_i32 s4, s3, 0x3000
	s_add_u32 s5, s14, s5
	v_mov_b32_e32 v166, v224
	s_addc_u32 s4, s15, s4
	s_lshl_b32 s18, s2, 8
	s_lshl_b32 s6, s2, 9
	s_add_u32 s5, s5, s6
	v_ashrrev_i32_e32 v24, 4, v166
	s_addc_u32 s6, s4, 0
	v_lshlrev_b32_e32 v23, 2, v24
	s_add_u32 s4, s5, 0x2000
	v_and_b32_e32 v1, 15, v166
	v_bitop3_b32 v8, v23, v166, 15 bitop3:0x78
	s_addc_u32 s5, s6, 0
	v_lshlrev_b32_e32 v8, 3, v8
	v_bitop3_b32 v14, v23, v1, 1 bitop3:0x36
	v_add_u32_e32 v2, s40, v24
	v_mov_b64_e32 v[4:5], s[4:5]
	v_ashrrev_i32_e32 v9, 31, v8
	v_lshlrev_b32_e32 v14, 3, v14
	v_bitop3_b32 v20, v23, v1, 2 bitop3:0x36
	v_mad_i64_i32 v[6:7], s[4:5], v2, s74, v[4:5]
	v_lshlrev_b64 v[8:9], 1, v[8:9]
	s_add_i32 s6, s41, 0
	v_add_u32_e32 v10, s42, v24
	v_ashrrev_i32_e32 v15, 31, v14
	v_lshlrev_b32_e32 v20, 3, v20
	v_bitop3_b32 v25, v23, v1, 3 bitop3:0x36
	v_lshl_add_u64 v[6:7], v[6:7], 0, v[8:9]
	s_mov_b32 m0, s6
	v_mad_i64_i32 v[12:13], s[4:5], v10, s74, v[4:5]
	v_lshlrev_b64 v[14:15], 1, v[14:15]
	s_add_i32 s7, s43, 0
	v_add_u32_e32 v16, s44, v24
	v_ashrrev_i32_e32 v21, 31, v20
	v_add_u32_e32 v22, s46, v24
	v_lshlrev_b32_e32 v26, 3, v25
	global_load_lds_dwordx4 v[6:7], off nt
	v_lshl_add_u64 v[12:13], v[12:13], 0, v[14:15]
	s_mov_b32 m0, s7
	v_mad_i64_i32 v[18:19], s[4:5], v16, s74, v[4:5]
	v_lshlrev_b64 v[20:21], 1, v[20:21]
	s_add_i32 s8, s45, 0
	v_mad_i64_i32 v[4:5], s[4:5], v22, s74, v[4:5]
	v_ashrrev_i32_e32 v27, 31, v26
	global_load_lds_dwordx4 v[12:13], off nt
	v_lshl_add_u64 v[18:19], v[18:19], 0, v[20:21]
	s_mov_b32 m0, s8
	v_lshlrev_b64 v[26:27], 1, v[26:27]
	s_add_i32 s4, s47, 0
	global_load_lds_dwordx4 v[18:19], off nt
	v_lshl_add_u64 v[4:5], v[4:5], 0, v[26:27]
	s_mov_b32 m0, s4
	v_lshl_add_u64 v[6:7], v[6:7], 0, s[20:21]
	global_load_lds_dwordx4 v[4:5], off nt
	s_add_i32 m0, s6, 0x8000
	v_ashrrev_i32_e32 v3, 31, v2
	global_load_lds_dwordx4 v[6:7], off nt
	v_lshl_add_u64 v[6:7], v[12:13], 0, s[20:21]
	s_add_i32 m0, s7, 0x8000
	v_ashrrev_i32_e32 v11, 31, v10
	global_load_lds_dwordx4 v[6:7], off nt
	v_lshl_add_u64 v[6:7], v[18:19], 0, s[20:21]
	s_add_i32 m0, s8, 0x8000
	v_lshl_add_u64 v[4:5], v[4:5], 0, s[20:21]
	global_load_lds_dwordx4 v[6:7], off nt
	s_add_i32 m0, s4, 0x8000
	v_lshlrev_b64 v[2:3], 9, v[2:3]
	v_ashrrev_i32_e32 v17, 31, v16
	global_load_lds_dwordx4 v[4:5], off nt
	v_lshl_add_u64 v[2:3], s[0:1], 0, v[2:3]
	v_lshlrev_b64 v[4:5], 9, v[10:11]
	v_ashrrev_i32_e32 v23, 31, v22
	v_lshl_add_u64 v[2:3], v[2:3], 0, v[8:9]
	s_add_i32 m0, s55, s41
	v_lshl_add_u64 v[4:5], s[0:1], 0, v[4:5]
	v_lshlrev_b64 v[6:7], 9, v[16:17]
	global_load_lds_dwordx4 v[2:3], off nt
	v_lshl_add_u64 v[4:5], v[4:5], 0, v[14:15]
	s_add_i32 m0, s55, s43
	v_lshl_add_u64 v[6:7], s[0:1], 0, v[6:7]
	v_lshlrev_b64 v[8:9], 9, v[22:23]
	global_load_lds_dwordx4 v[4:5], off nt
	v_lshl_add_u64 v[6:7], v[6:7], 0, v[20:21]
	s_add_i32 m0, s55, s45
	v_lshl_add_u64 v[8:9], s[0:1], 0, v[8:9]
	global_load_lds_dwordx4 v[6:7], off nt
	v_lshl_add_u64 v[8:9], v[8:9], 0, v[26:27]
	s_add_i32 m0, s55, s47
	v_and_b32_e32 v158, 31, v166
	global_load_lds_dwordx4 v[8:9], off nt
	v_lshl_add_u64 v[2:3], v[2:3], 0, s[20:21]
	s_add_i32 m0, s56, s41
	v_or_b32_e32 v172, s48, v158
	global_load_lds_dwordx4 v[2:3], off nt
	v_lshl_add_u64 v[2:3], v[4:5], 0, s[20:21]
	s_add_i32 m0, s56, s43
	v_or_b32_e32 v170, s3, v172
	global_load_lds_dwordx4 v[2:3], off nt
	v_lshl_add_u64 v[2:3], v[6:7], 0, s[20:21]
	s_add_i32 m0, s56, s45
	v_ashrrev_i32_e32 v171, 31, v170
	global_load_lds_dwordx4 v[2:3], off nt
	v_lshl_add_u64 v[2:3], v[8:9], 0, s[20:21]
	s_add_i32 m0, s56, s47
	v_ashrrev_i32_e32 v157, 5, v166
	global_load_lds_dwordx4 v[2:3], off nt
	v_lshlrev_b64 v[2:3], 10, v[170:171]
	v_lshl_add_u64 v[2:3], s[12:13], 0, v[2:3]
	v_lshlrev_b32_e32 v168, 3, v157
	v_lshl_add_u64 v[2:3], v[2:3], 0, s[18:19]
	v_ashrrev_i32_e32 v169, 31, v168
	v_add_u32_e32 v8, s27, v166
	v_lshl_add_u64 v[2:3], v[168:169], 1, v[2:3]
	v_ashrrev_i32_e32 v114, 4, v8
	v_add_u32_e32 v6, 0x200, v8
	global_load_dwordx4 v[82:85], v[2:3], off nt
	global_load_dwordx4 v[86:89], v[2:3], off offset:32 nt
	global_load_dwordx4 v[90:93], v[2:3], off offset:64 nt
	global_load_dwordx4 v[94:97], v[2:3], off offset:96 nt
	global_load_dwordx4 v[98:101], v[2:3], off offset:128 nt
	global_load_dwordx4 v[102:105], v[2:3], off offset:160 nt
	global_load_dwordx4 v[106:109], v[2:3], off offset:192 nt
	global_load_dwordx4 v[110:113], v[2:3], off offset:224 nt
	s_add_u32 s0, s49, s18
	v_lshlrev_b32_e32 v2, 4, v166
	v_add_u32_e32 v4, s3, v114
	v_ashrrev_i32_e32 v115, 4, v6
	s_addc_u32 s1, s50, 0
	v_and_b32_e32 v162, 0xf0, v2
	v_ashrrev_i32_e32 v5, 31, v4
	v_add_u32_e32 v6, s3, v115
	v_lshl_add_u64 v[2:3], s[0:1], 0, v[162:163]
	v_lshlrev_b64 v[4:5], 10, v[4:5]
	v_ashrrev_i32_e32 v7, 31, v6
	v_lshl_add_u64 v[4:5], v[2:3], 0, v[4:5]
	v_lshlrev_b64 v[6:7], 10, v[6:7]
	v_lshl_add_u64 v[6:7], v[2:3], 0, v[6:7]
	global_load_dwordx4 v[74:77], v[4:5], off nt
	global_load_dwordx4 v[66:69], v[6:7], off nt
	v_add_u32_e32 v4, 0x400, v8
	v_ashrrev_i32_e32 v116, 4, v4
	v_add_u32_e32 v6, 0x600, v8
	v_add_u32_e32 v4, s3, v116
	v_ashrrev_i32_e32 v117, 4, v6
	v_ashrrev_i32_e32 v5, 31, v4
	v_add_u32_e32 v6, s3, v117
	v_lshlrev_b64 v[4:5], 10, v[4:5]
	v_ashrrev_i32_e32 v7, 31, v6
	v_lshl_add_u64 v[4:5], v[2:3], 0, v[4:5]
	v_lshlrev_b64 v[6:7], 10, v[6:7]
	v_lshl_add_u64 v[2:3], v[2:3], 0, v[6:7]
	global_load_dwordx4 v[78:81], v[4:5], off nt
	global_load_dwordx4 v[70:73], v[2:3], off nt
	v_readlane_b32 s0, v254, 23
	s_cmp_lt_i32 s0, 1
	s_mov_b64 s[0:1], -1
	s_cbranch_scc1 .LBB0_682
	v_readlane_b32 s0, v254, 23
	s_cmp_eq_u32 s0, 1
	s_cbranch_scc0 .LBB0_681
	s_lshl_b64 s[0:1], s[36:37], 9
	s_add_u32 s0, s51, s0
	s_addc_u32 s1, s52, s1
	v_ashrrev_i32_e32 v167, 31, v166
	v_lshl_add_u64 v[2:3], v[166:167], 2, s[0:1]
	global_load_dword v4, v[2:3], off
	s_nop 0
	global_load_dword v2, v[2:3], off offset:256
	s_add_i32 s0, 0, 0x20000
	v_lshl_add_u32 v3, v166, 2, s0
	s_waitcnt vmcnt(0)
	ds_write2st64_b32 v3, v4, v2 offset0:8 offset1:9

; DI f32x16 mfma32(bf16x8 a, bf16x8 b, f32x16 c) { return __builtin_amdgcn_mfma_f32_32x32x16_bf16(a, b, c, 0, 0, 0); }
; DI int tr_base(int rlane, int cch, int q, int p) { return img_off(rlane + q, cch + (p >> 1)) + 8 * (p & 1); }
; DI bf16x8 tr_frag2(const LAS unsigned char* img, int ba, int bb, int off) { const s16x4 lo = tr16(img + ba + off), hi = tr16(img + bb + off); return __builtin_shufflevector(lo, hi, 0, 1, 2, 3, 4, 5, 6, 7); }
; DI void mlstm_m3_unit(Frame& F, int u) {
;     ...
;     int cB0[4], cB1[4];
; #pragma unroll
;     for (int nb = 0; nb < 4; ++nb) { cB0[nb] = tr_base(8 * h, 4 * nb + 2 * (g & 1), q4, p4); cB1[nb] = tr_base(8 * h + 4, 4 * nb + 2 * (g & 1), q4, p4); }
; #pragma unroll
;     for (int kk = 0; kk < 8; ++kk) {
; #pragma unroll
;         for (int nb = 0; nb < 4; ++nb) { const bf16x8 a = tr_frag2(imgC, cB0[nb], cB1[nb], kk * 4096);
;             acc[nb] = mfma32(a, qf[kk], acc[nb]); }
;         __builtin_amdgcn_sched_barrier(0);
;     }
.LBB0_684:
	v_bfe_u32 v160, v166, 2, 2
	v_lshlrev_b32_e32 v2, 1, v24
	v_or_b32_e32 v3, v160, v168
	v_bfe_u32 v4, v166, 1, 1
	s_waitcnt vmcnt(0)
	v_and_or_b32 v147, v2, 2, v4
	v_lshlrev_b32_e32 v2, 2, v3
	v_and_b32_e32 v22, 12, v2
	v_lshrrev_b32_e32 v2, 2, v168
	v_and_b32_e32 v23, 2, v2
	v_lshlrev_b32_e32 v2, 3, v166
	v_and_b32_e32 v177, 8, v2
	v_or_b32_e32 v2, 4, v168
	v_lshl_or_b32 v38, v3, 8, v177
	v_or_b32_e32 v3, v2, v160
	v_lshlrev_b32_e32 v4, 2, v3
	v_and_b32_e32 v39, 12, v4
	v_bfe_u32 v40, v2, 2, 2
	v_bitop3_b32 v2, v22, v147, v23 bitop3:0x36
	v_lshl_or_b32 v41, v3, 8, v177
	v_lshl_or_b32 v126, v2, 4, v38
	v_bitop3_b32 v2, v39, v147, v40 bitop3:0x36
	v_or_b32_e32 v148, 4, v147
	v_or_b32_e32 v149, 8, v147
	v_or_b32_e32 v150, 12, v147
	v_lshl_or_b32 v127, v2, 4, v41
	v_bitop3_b32 v2, v22, v148, v23 bitop3:0x36
	v_bitop3_b32 v6, v22, v149, v23 bitop3:0x36
	v_bitop3_b32 v42, v22, v150, v23 bitop3:0x36
	v_lshl_or_b32 v128, v2, 4, v38
	v_bitop3_b32 v2, v39, v148, v40 bitop3:0x36
	v_lshl_or_b32 v130, v6, 4, v38
	v_bitop3_b32 v24, v39, v149, v40 bitop3:0x36
	v_lshl_or_b32 v132, v42, 4, v38
	v_bitop3_b32 v38, v39, v150, v40 bitop3:0x36
	v_lshl_or_b32 v129, v2, 4, v41
	v_add_u32_e32 v2, s57, v126
	v_add_u32_e32 v4, s57, v127
	v_add_u32_e32 v6, s57, v128
	v_lshl_or_b32 v131, v24, 4, v41
	v_add_u32_e32 v22, s57, v130
	v_lshl_or_b32 v133, v38, 4, v41
	v_add_u32_e32 v38, s57, v132
	s_waitcnt vmcnt(4)
	s_waitcnt lgkmcnt(0)
	s_barrier
	ds_read_b64_tr_b16 v[2:3], v2
	ds_read_b64_tr_b16 v[4:5], v4
	v_add_u32_e32 v7, s57, v129
	ds_read_b64_tr_b16 v[18:19], v6
	ds_read_b64_tr_b16 v[20:21], v7
	v_add_u32_e32 v23, s57, v131
	ds_read_b64_tr_b16 v[34:35], v22
	ds_read_b64_tr_b16 v[36:37], v23
	v_add_u32_e32 v39, s57, v133
	ds_read_b64_tr_b16 v[50:51], v38
	ds_read_b64_tr_b16 v[52:53], v39
	s_waitcnt lgkmcnt(6)
	v_mfma_f32_32x32x16_bf16 v[2:17], v[2:5], v[82:85], 0
	s_mov_b32 s0, 0
	s_waitcnt lgkmcnt(4)
	v_mfma_f32_32x32x16_bf16 v[18:33], v[18:21], v[82:85], 0
	s_waitcnt lgkmcnt(2)
	v_mfma_f32_32x32x16_bf16 v[34:49], v[34:37], v[82:85], 0
	s_waitcnt lgkmcnt(0)
	v_mfma_f32_32x32x16_bf16 v[50:65], v[50:53], v[82:85], 0
	v_add_u32_e32 v118, s58, v126
	v_add_u32_e32 v120, s58, v127
	v_add_u32_e32 v122, s58, v128
	v_add_u32_e32 v124, s58, v129
	ds_read_b64_tr_b16 v[118:119], v118
	ds_read_b64_tr_b16 v[120:121], v120
	ds_read_b64_tr_b16 v[122:123], v122
	ds_read_b64_tr_b16 v[124:125], v124
	s_waitcnt lgkmcnt(2)
	v_mfma_f32_32x32x16_bf16 v[2:17], v[118:121], v[86:89], v[2:17]
	v_add_u32_e32 v118, s58, v130
	v_add_u32_e32 v120, s58, v131
	ds_read_b64_tr_b16 v[118:119], v118
	ds_read_b64_tr_b16 v[120:121], v120
	s_waitcnt lgkmcnt(2)
	v_mfma_f32_32x32x16_bf16 v[18:33], v[122:125], v[86:89], v[18:33]
	v_add_u32_e32 v122, s58, v132
	v_add_u32_e32 v124, s58, v133
	ds_read_b64_tr_b16 v[122:123], v122
	ds_read_b64_tr_b16 v[124:125], v124
	s_waitcnt lgkmcnt(2)
	v_mfma_f32_32x32x16_bf16 v[34:49], v[118:121], v[86:89], v[34:49]
	s_waitcnt lgkmcnt(0)
	v_mfma_f32_32x32x16_bf16 v[50:65], v[122:125], v[86:89], v[50:65]
	v_add_u32_e32 v118, s59, v126
	v_add_u32_e32 v120, s59, v127
	v_add_u32_e32 v122, s59, v128
	v_add_u32_e32 v124, s59, v129
	ds_read_b64_tr_b16 v[118:119], v118
	ds_read_b64_tr_b16 v[120:121], v120
	ds_read_b64_tr_b16 v[122:123], v122
	ds_read_b64_tr_b16 v[124:125], v124
	s_waitcnt lgkmcnt(2)
	v_mfma_f32_32x32x16_bf16 v[2:17], v[118:121], v[90:93], v[2:17]
	v_add_u32_e32 v118, s59, v130
	v_add_u32_e32 v120, s59, v131
	ds_read_b64_tr_b16 v[118:119], v118
	ds_read_b64_tr_b16 v[120:121], v120
	s_waitcnt lgkmcnt(2)
	v_mfma_f32_32x32x16_bf16 v[18:33], v[122:125], v[90:93], v[18:33]
	v_add_u32_e32 v122, s59, v132
	v_add_u32_e32 v124, s59, v133
	ds_read_b64_tr_b16 v[122:123], v122
	ds_read_b64_tr_b16 v[124:125], v124
	s_waitcnt lgkmcnt(2)
	v_mfma_f32_32x32x16_bf16 v[34:49], v[118:121], v[90:93], v[34:49]
	s_waitcnt lgkmcnt(0)
	v_mfma_f32_32x32x16_bf16 v[50:65], v[122:125], v[90:93], v[50:65]
	v_add_u32_e32 v118, s60, v126
	v_add_u32_e32 v120, s60, v127
	v_add_u32_e32 v122, s60, v128
	v_add_u32_e32 v124, s60, v129
	ds_read_b64_tr_b16 v[118:119], v118
	ds_read_b64_tr_b16 v[120:121], v120
	ds_read_b64_tr_b16 v[122:123], v122
	ds_read_b64_tr_b16 v[124:125], v124
	s_waitcnt lgkmcnt(2)
	v_mfma_f32_32x32x16_bf16 v[2:17], v[118:121], v[94:97], v[2:17]
	v_add_u32_e32 v118, s60, v130
	v_add_u32_e32 v120, s60, v131
	ds_read_b64_tr_b16 v[118:119], v118
	ds_read_b64_tr_b16 v[120:121], v120
	s_waitcnt lgkmcnt(2)
	v_mfma_f32_32x32x16_bf16 v[18:33], v[122:125], v[94:97], v[18:33]
	v_add_u32_e32 v122, s60, v132
	v_add_u32_e32 v124, s60, v133
	ds_read_b64_tr_b16 v[122:123], v122
	ds_read_b64_tr_b16 v[124:125], v124
	s_waitcnt lgkmcnt(2)
	v_mfma_f32_32x32x16_bf16 v[34:49], v[118:121], v[94:97], v[34:49]
	s_waitcnt lgkmcnt(0)
	v_mfma_f32_32x32x16_bf16 v[50:65], v[122:125], v[94:97], v[50:65]
	v_add_u32_e32 v118, s61, v126
	v_add_u32_e32 v120, s61, v127
	v_add_u32_e32 v122, s61, v128
	v_add_u32_e32 v124, s61, v129
	ds_read_b64_tr_b16 v[118:119], v118
	ds_read_b64_tr_b16 v[120:121], v120
	ds_read_b64_tr_b16 v[122:123], v122
	ds_read_b64_tr_b16 v[124:125], v124
	s_waitcnt lgkmcnt(2)
	v_mfma_f32_32x32x16_bf16 v[2:17], v[118:121], v[98:101], v[2:17]
	v_add_u32_e32 v118, s61, v130
	v_add_u32_e32 v120, s61, v131
	ds_read_b64_tr_b16 v[118:119], v118
	ds_read_b64_tr_b16 v[120:121], v120
	s_waitcnt lgkmcnt(2)
	v_mfma_f32_32x32x16_bf16 v[18:33], v[122:125], v[98:101], v[18:33]
	v_add_u32_e32 v122, s61, v132
	v_add_u32_e32 v124, s61, v133
	ds_read_b64_tr_b16 v[122:123], v122
	ds_read_b64_tr_b16 v[124:125], v124
	s_waitcnt lgkmcnt(2)
	v_mfma_f32_32x32x16_bf16 v[34:49], v[118:121], v[98:101], v[34:49]
	s_waitcnt lgkmcnt(0)
; #define LAS __attribute__((address_space(3)))
; DI f32x16 mfma32(bf16x8 a, bf16x8 b, f32x16 c) { return __builtin_amdgcn_mfma_f32_32x32x16_bf16(a, b, c, 0, 0, 0); }
; DI bf16x8 tr_frag2(const LAS unsigned char* img, int ba, int bb, int off) { const s16x4 lo = tr16(img + ba + off), hi = tr16(img + bb + off); return __builtin_shufflevector(lo, hi, 0, 1, 2, 3, 4, 5, 6, 7); }
; DI void mlstm_m3_unit(Frame& F, int u) {
;     ...
;         for (int nb = 0; nb < 4; ++nb) { const bf16x8 a = tr_frag2(imgC, cB0[nb], cB1[nb], kk * 4096);
;             acc[nb] = mfma32(a, qf[kk], acc[nb]); }
;         __builtin_amdgcn_sched_barrier(0);
;     }
;     const float wi = mf[256 + tl], Mt = mf[128 + tl], en = mf[384 + tl];
; #pragma unroll
;     for (int nb = 0; nb < 4; ++nb)
; #pragma unroll
;         for (int e = 0; e < 16; ++e) acc[nb][e] *= wi;
;     float qn = 0.f;
; #pragma unroll
;     for (int kk = 0; kk < 8; ++kk) { const f32x4 n0 = *(const LAS f32x4*)(mf + 512 + 16 * kk + 8 * h), n1 = *(const LAS f32x4*)(mf + 512 + 16 * kk + 8 * h + 4);
;         const u32x4 qq = __builtin_bit_cast(u32x4, qf[kk]);
;         qn += __uint_as_float(qq[0] << 16) * n0[0] + __uint_as_float(qq[0] & 0xffff0000u) * n0[1] + __uint_as_float(qq[1] << 16) * n0[2] + __uint_as_float(qq[1] & 0xffff0000u) * n0[3];
;         qn += __uint_as_float(qq[2] << 16) * n1[0] + __uint_as_float(qq[2] & 0xffff0000u) * n1[1] + __uint_as_float(qq[3] << 16) * n1[2] + __uint_as_float(qq[3] & 0xffff0000u) * n1[3]; }
	v_mfma_f32_32x32x16_bf16 v[50:65], v[122:125], v[98:101], v[50:65]
	v_add_u32_e32 v118, s62, v126
	v_add_u32_e32 v120, s62, v127
	v_add_u32_e32 v122, s62, v128
	v_add_u32_e32 v124, s62, v129
	ds_read_b64_tr_b16 v[118:119], v118
	ds_read_b64_tr_b16 v[120:121], v120
	ds_read_b64_tr_b16 v[122:123], v122
	ds_read_b64_tr_b16 v[124:125], v124
	s_waitcnt lgkmcnt(2)
	v_mfma_f32_32x32x16_bf16 v[2:17], v[118:121], v[102:105], v[2:17]
	v_add_u32_e32 v118, s62, v130
	v_add_u32_e32 v120, s62, v131
	ds_read_b64_tr_b16 v[118:119], v118
	ds_read_b64_tr_b16 v[120:121], v120
	s_waitcnt lgkmcnt(2)
	v_mfma_f32_32x32x16_bf16 v[18:33], v[122:125], v[102:105], v[18:33]
	v_add_u32_e32 v122, s62, v132
	v_add_u32_e32 v124, s62, v133
	ds_read_b64_tr_b16 v[122:123], v122
	ds_read_b64_tr_b16 v[124:125], v124
	s_waitcnt lgkmcnt(2)
	v_mfma_f32_32x32x16_bf16 v[34:49], v[118:121], v[102:105], v[34:49]
	s_waitcnt lgkmcnt(0)
	v_mfma_f32_32x32x16_bf16 v[50:65], v[122:125], v[102:105], v[50:65]
	v_add_u32_e32 v118, s63, v126
	v_add_u32_e32 v120, s63, v127
	v_add_u32_e32 v122, s63, v128
	v_add_u32_e32 v124, s63, v129
	ds_read_b64_tr_b16 v[118:119], v118
	ds_read_b64_tr_b16 v[120:121], v120
	ds_read_b64_tr_b16 v[122:123], v122
	ds_read_b64_tr_b16 v[124:125], v124
	s_waitcnt lgkmcnt(2)
	v_mfma_f32_32x32x16_bf16 v[2:17], v[118:121], v[106:109], v[2:17]
	v_add_u32_e32 v118, s63, v130
	v_add_u32_e32 v120, s63, v131
	ds_read_b64_tr_b16 v[118:119], v118
	ds_read_b64_tr_b16 v[120:121], v120
	s_waitcnt lgkmcnt(2)
	v_mfma_f32_32x32x16_bf16 v[18:33], v[122:125], v[106:109], v[18:33]
	v_add_u32_e32 v122, s63, v132
	v_add_u32_e32 v124, s63, v133
	ds_read_b64_tr_b16 v[122:123], v122
	ds_read_b64_tr_b16 v[124:125], v124
	s_waitcnt lgkmcnt(2)
	v_mfma_f32_32x32x16_bf16 v[34:49], v[118:121], v[106:109], v[34:49]
	s_waitcnt lgkmcnt(0)
	v_mfma_f32_32x32x16_bf16 v[50:65], v[122:125], v[106:109], v[50:65]
	v_add_u32_e32 v118, s64, v126
	v_add_u32_e32 v120, s64, v127
	v_add_u32_e32 v122, s64, v128
	v_add_u32_e32 v124, s64, v129
	ds_read_b64_tr_b16 v[118:119], v118
	ds_read_b64_tr_b16 v[120:121], v120
	ds_read_b64_tr_b16 v[122:123], v122
	ds_read_b64_tr_b16 v[124:125], v124
	s_waitcnt lgkmcnt(2)
	v_mfma_f32_32x32x16_bf16 v[2:17], v[118:121], v[110:113], v[2:17]
	v_add_u32_e32 v118, s64, v130
	v_add_u32_e32 v120, s64, v131
	ds_read_b64_tr_b16 v[118:119], v118
	ds_read_b64_tr_b16 v[120:121], v120
	s_waitcnt lgkmcnt(2)
	v_mfma_f32_32x32x16_bf16 v[18:33], v[122:125], v[110:113], v[18:33]
	v_add_u32_e32 v122, s64, v132
	v_add_u32_e32 v124, s64, v133
	ds_read_b64_tr_b16 v[122:123], v122
	ds_read_b64_tr_b16 v[124:125], v124
	s_waitcnt lgkmcnt(2)
	v_mfma_f32_32x32x16_bf16 v[34:49], v[118:121], v[110:113], v[34:49]
	s_waitcnt lgkmcnt(0)
	v_mfma_f32_32x32x16_bf16 v[50:65], v[122:125], v[110:113], v[50:65]
	s_add_i32 s1, 0, 0x20000
	v_lshl_add_u32 v162, v172, 2, s1
	ds_read2st64_b32 v[174:175], v162 offset0:2 offset1:4
	v_lshl_add_u32 v118, v168, 2, 0
	v_add_u32_e32 v126, 0x20800, v118
	ds_read_b32 v167, v162 offset:1536
	ds_read_b128 v[118:121], v126
	v_and_b32_e32 v128, 0xffff0000, v82
	s_waitcnt lgkmcnt(2)
	v_mov_b32_e32 v122, v175
	v_pk_mul_f32 v[16:17], v[16:17], v[122:123] op_sel_hi:[1,0]
	v_pk_mul_f32 v[14:15], v[14:15], v[122:123] op_sel_hi:[1,0]
	v_pk_mul_f32 v[12:13], v[12:13], v[122:123] op_sel_hi:[1,0]
	v_pk_mul_f32 v[10:11], v[10:11], v[122:123] op_sel_hi:[1,0]
	v_pk_mul_f32 v[8:9], v[8:9], v[122:123] op_sel_hi:[1,0]
	v_pk_mul_f32 v[6:7], v[6:7], v[122:123] op_sel_hi:[1,0]
	v_pk_mul_f32 v[4:5], v[4:5], v[122:123] op_sel_hi:[1,0]
	v_pk_mul_f32 v[2:3], v[2:3], v[122:123] op_sel_hi:[1,0]
	v_pk_mul_f32 v[32:33], v[32:33], v[122:123] op_sel_hi:[1,0]
	v_pk_mul_f32 v[30:31], v[30:31], v[122:123] op_sel_hi:[1,0]
	v_pk_mul_f32 v[28:29], v[28:29], v[122:123] op_sel_hi:[1,0]
	v_pk_mul_f32 v[26:27], v[26:27], v[122:123] op_sel_hi:[1,0]
	v_pk_mul_f32 v[24:25], v[24:25], v[122:123] op_sel_hi:[1,0]
	v_pk_mul_f32 v[22:23], v[22:23], v[122:123] op_sel_hi:[1,0]
	v_pk_mul_f32 v[20:21], v[20:21], v[122:123] op_sel_hi:[1,0]
	v_pk_mul_f32 v[18:19], v[18:19], v[122:123] op_sel_hi:[1,0]
	v_pk_mul_f32 v[48:49], v[48:49], v[122:123] op_sel_hi:[1,0]
	v_pk_mul_f32 v[46:47], v[46:47], v[122:123] op_sel_hi:[1,0]
	v_pk_mul_f32 v[44:45], v[44:45], v[122:123] op_sel_hi:[1,0]
	v_pk_mul_f32 v[42:43], v[42:43], v[122:123] op_sel_hi:[1,0]
	v_pk_mul_f32 v[40:41], v[40:41], v[122:123] op_sel_hi:[1,0]
	v_pk_mul_f32 v[38:39], v[38:39], v[122:123] op_sel_hi:[1,0]
	v_pk_mul_f32 v[36:37], v[36:37], v[122:123] op_sel_hi:[1,0]
	v_pk_mul_f32 v[34:35], v[34:35], v[122:123] op_sel_hi:[1,0]
	v_pk_mul_f32 v[64:65], v[64:65], v[122:123] op_sel_hi:[1,0]
	v_pk_mul_f32 v[62:63], v[62:63], v[122:123] op_sel_hi:[1,0]
	v_pk_mul_f32 v[60:61], v[60:61], v[122:123] op_sel_hi:[1,0]
	v_pk_mul_f32 v[58:59], v[58:59], v[122:123] op_sel_hi:[1,0]
	v_pk_mul_f32 v[56:57], v[56:57], v[122:123] op_sel_hi:[1,0]
	v_pk_mul_f32 v[54:55], v[54:55], v[122:123] op_sel_hi:[1,0]
	v_pk_mul_f32 v[52:53], v[52:53], v[122:123] op_sel_hi:[1,0]
	v_pk_mul_f32 v[50:51], v[50:51], v[122:123] op_sel_hi:[1,0]
	ds_read_b128 v[122:125], v126 offset:16
	v_lshlrev_b32_e32 v127, 16, v82
	s_waitcnt lgkmcnt(1)
	v_mul_f32_e32 v119, v119, v128
	v_fmac_f32_e32 v119, v118, v127
	v_lshlrev_b32_e32 v118, 16, v83
	v_fmac_f32_e32 v119, v120, v118
	v_and_b32_e32 v118, 0xffff0000, v83
	v_fmac_f32_e32 v119, v121, v118
	v_and_b32_e32 v129, 0xffff0000, v84
	v_add_f32_e32 v127, 0, v119
	v_lshlrev_b32_e32 v128, 16, v84
	ds_read_b128 v[118:121], v126 offset:64
	s_waitcnt lgkmcnt(1)
; #define LAS __attribute__((address_space(3)))
; DI void mlstm_m3_unit(Frame& F, int u) {
;     ...
;     float qn = 0.f;
; #pragma unroll
;     for (int kk = 0; kk < 8; ++kk) { const f32x4 n0 = *(const LAS f32x4*)(mf + 512 + 16 * kk + 8 * h), n1 = *(const LAS f32x4*)(mf + 512 + 16 * kk + 8 * h + 4);
;         const u32x4 qq = __builtin_bit_cast(u32x4, qf[kk]);
;         qn += __uint_as_float(qq[0] << 16) * n0[0] + __uint_as_float(qq[0] & 0xffff0000u) * n0[1] + __uint_as_float(qq[1] << 16) * n0[2] + __uint_as_float(qq[1] & 0xffff0000u) * n0[3];
;         qn += __uint_as_float(qq[2] << 16) * n1[0] + __uint_as_float(qq[2] & 0xffff0000u) * n1[1] + __uint_as_float(qq[3] << 16) * n1[2] + __uint_as_float(qq[3] & 0xffff0000u) * n1[3]; }
;     qn += __shfl_xor(qn, 32);
;     __syncthreads();
	v_mul_f32_e32 v123, v123, v129
	v_fmac_f32_e32 v123, v122, v128
	v_lshlrev_b32_e32 v122, 16, v85
	v_fmac_f32_e32 v123, v124, v122
	v_and_b32_e32 v122, 0xffff0000, v85
	v_fmac_f32_e32 v123, v125, v122
	v_add_f32_e32 v127, v123, v127
	ds_read_b128 v[122:125], v126 offset:80
	v_and_b32_e32 v129, 0xffff0000, v86
	v_lshlrev_b32_e32 v128, 16, v86
	s_waitcnt lgkmcnt(1)
	v_mul_f32_e32 v119, v119, v129
	v_fmac_f32_e32 v119, v118, v128
	v_lshlrev_b32_e32 v118, 16, v87
	v_fmac_f32_e32 v119, v120, v118
	v_and_b32_e32 v118, 0xffff0000, v87
	v_fmac_f32_e32 v119, v121, v118
	v_and_b32_e32 v129, 0xffff0000, v88
	v_add_f32_e32 v127, v127, v119
	v_lshlrev_b32_e32 v128, 16, v88
	ds_read_b128 v[118:121], v126 offset:128
	s_waitcnt lgkmcnt(1)
	v_mul_f32_e32 v123, v123, v129
	v_fmac_f32_e32 v123, v122, v128
	v_lshlrev_b32_e32 v122, 16, v89
	v_fmac_f32_e32 v123, v124, v122
	v_and_b32_e32 v122, 0xffff0000, v89
	v_fmac_f32_e32 v123, v125, v122
	v_add_f32_e32 v127, v123, v127
	ds_read_b128 v[122:125], v126 offset:144
	v_and_b32_e32 v129, 0xffff0000, v90
	v_lshlrev_b32_e32 v128, 16, v90
	s_waitcnt lgkmcnt(1)
	v_mul_f32_e32 v119, v119, v129
	v_fmac_f32_e32 v119, v118, v128
	v_lshlrev_b32_e32 v118, 16, v91
	v_fmac_f32_e32 v119, v120, v118
	v_and_b32_e32 v118, 0xffff0000, v91
	v_fmac_f32_e32 v119, v121, v118
	v_and_b32_e32 v129, 0xffff0000, v92
	v_add_f32_e32 v127, v127, v119
	v_lshlrev_b32_e32 v128, 16, v92
	ds_read_b128 v[118:121], v126 offset:192
	s_waitcnt lgkmcnt(1)
	v_mul_f32_e32 v123, v123, v129
	v_fmac_f32_e32 v123, v122, v128
	v_lshlrev_b32_e32 v122, 16, v93
	v_fmac_f32_e32 v123, v124, v122
	v_and_b32_e32 v122, 0xffff0000, v93
	v_fmac_f32_e32 v123, v125, v122
	v_add_f32_e32 v127, v123, v127
	ds_read_b128 v[122:125], v126 offset:208
	v_and_b32_e32 v129, 0xffff0000, v94
	v_lshlrev_b32_e32 v128, 16, v94
	s_waitcnt lgkmcnt(1)
	v_mul_f32_e32 v119, v119, v129
	v_fmac_f32_e32 v119, v118, v128
	v_lshlrev_b32_e32 v118, 16, v95
	v_fmac_f32_e32 v119, v120, v118
	v_and_b32_e32 v118, 0xffff0000, v95
	v_fmac_f32_e32 v119, v121, v118
	v_and_b32_e32 v129, 0xffff0000, v96
	v_add_f32_e32 v127, v127, v119
	v_lshlrev_b32_e32 v128, 16, v96
	ds_read_b128 v[118:121], v126 offset:256
	s_waitcnt lgkmcnt(1)
	v_mul_f32_e32 v123, v123, v129
	v_fmac_f32_e32 v123, v122, v128
	v_lshlrev_b32_e32 v122, 16, v97
	v_fmac_f32_e32 v123, v124, v122
	v_and_b32_e32 v122, 0xffff0000, v97
	v_fmac_f32_e32 v123, v125, v122
	v_add_f32_e32 v127, v123, v127
	ds_read_b128 v[122:125], v126 offset:272
	v_and_b32_e32 v129, 0xffff0000, v98
	v_lshlrev_b32_e32 v128, 16, v98
	s_waitcnt lgkmcnt(1)
	v_mul_f32_e32 v119, v119, v129
	v_fmac_f32_e32 v119, v118, v128
	v_lshlrev_b32_e32 v118, 16, v99
	v_fmac_f32_e32 v119, v120, v118
	v_and_b32_e32 v118, 0xffff0000, v99
	v_fmac_f32_e32 v119, v121, v118
	v_and_b32_e32 v129, 0xffff0000, v100
	v_add_f32_e32 v127, v127, v119
	v_lshlrev_b32_e32 v128, 16, v100
	ds_read_b128 v[118:121], v126 offset:320
	s_waitcnt lgkmcnt(1)
	v_mul_f32_e32 v123, v123, v129
	v_fmac_f32_e32 v123, v122, v128
	v_lshlrev_b32_e32 v122, 16, v101
	v_fmac_f32_e32 v123, v124, v122
	v_and_b32_e32 v122, 0xffff0000, v101
	v_fmac_f32_e32 v123, v125, v122
	v_add_f32_e32 v127, v123, v127
	ds_read_b128 v[122:125], v126 offset:336
	v_and_b32_e32 v129, 0xffff0000, v102
	v_lshlrev_b32_e32 v128, 16, v102
	s_waitcnt lgkmcnt(1)
	v_mul_f32_e32 v119, v119, v129
	v_fmac_f32_e32 v119, v118, v128
	v_lshlrev_b32_e32 v118, 16, v103
	v_fmac_f32_e32 v119, v120, v118
	v_and_b32_e32 v118, 0xffff0000, v103
	v_fmac_f32_e32 v119, v121, v118
	v_and_b32_e32 v129, 0xffff0000, v104
	v_add_f32_e32 v127, v127, v119
	v_lshlrev_b32_e32 v128, 16, v104
	ds_read_b128 v[118:121], v126 offset:384
	s_waitcnt lgkmcnt(1)
	v_mul_f32_e32 v123, v123, v129
	v_fmac_f32_e32 v123, v122, v128
	v_lshlrev_b32_e32 v122, 16, v105
	v_fmac_f32_e32 v123, v124, v122
	v_and_b32_e32 v122, 0xffff0000, v105
	v_fmac_f32_e32 v123, v125, v122
	v_add_f32_e32 v127, v123, v127
	ds_read_b128 v[122:125], v126 offset:400
	v_and_b32_e32 v129, 0xffff0000, v106
	v_lshlrev_b32_e32 v128, 16, v106
	s_waitcnt lgkmcnt(1)
	v_mul_f32_e32 v119, v119, v129
	v_fmac_f32_e32 v119, v118, v128
	v_lshlrev_b32_e32 v118, 16, v107
	v_fmac_f32_e32 v119, v120, v118
	v_and_b32_e32 v118, 0xffff0000, v107
	v_fmac_f32_e32 v119, v121, v118
	v_and_b32_e32 v129, 0xffff0000, v108
	v_add_f32_e32 v127, v127, v119
	v_lshlrev_b32_e32 v128, 16, v108
	ds_read_b128 v[118:121], v126 offset:448
	s_waitcnt lgkmcnt(1)
	v_mul_f32_e32 v123, v123, v129
	v_fmac_f32_e32 v123, v122, v128
	v_lshlrev_b32_e32 v122, 16, v109
	v_fmac_f32_e32 v123, v124, v122
	v_and_b32_e32 v122, 0xffff0000, v109
	v_fmac_f32_e32 v123, v125, v122
	v_add_f32_e32 v127, v123, v127
	ds_read_b128 v[122:125], v126 offset:464
	v_and_b32_e32 v128, 0xffff0000, v110
	v_lshlrev_b32_e32 v126, 16, v110
	s_waitcnt lgkmcnt(1)
	v_mul_f32_e32 v119, v119, v128
	v_fmac_f32_e32 v119, v118, v126
	v_lshlrev_b32_e32 v118, 16, v111
	v_fmac_f32_e32 v119, v120, v118
	v_and_b32_e32 v118, 0xffff0000, v111
	v_fmac_f32_e32 v119, v121, v118
	v_and_b32_e32 v120, 0xffff0000, v112
	v_add_f32_e32 v118, v127, v119
	v_lshlrev_b32_e32 v119, 16, v112
	s_waitcnt lgkmcnt(0)
	v_mul_f32_e32 v120, v123, v120
	v_fmac_f32_e32 v120, v122, v119
	v_lshlrev_b32_e32 v119, 16, v113
	v_fmac_f32_e32 v120, v124, v119
	v_and_b32_e32 v119, 0xffff0000, v113
	v_fmac_f32_e32 v120, v125, v119
	v_and_b32_e32 v119, 64, v211
	v_add_f32_e32 v176, v120, v118
	v_xor_b32_e32 v118, 32, v211
	v_add_u32_e32 v119, 64, v119
	v_cmp_lt_i32_e32 vcc, v118, v119
	v_lshlrev_b32_e32 v119, 2, v114
	v_and_b32_e32 v119, 12, v119
	v_cndmask_b32_e32 v118, v211, v118, vcc
	v_lshlrev_b32_e32 v213, 2, v118
	v_lshlrev_b32_e32 v118, 8, v114
	v_bfe_u32 v114, v114, 2, 2
	v_bitop3_b32 v114, v119, v1, v114 bitop3:0x36
	v_lshlrev_b32_e32 v114, 4, v114
	v_add3_u32 v114, s55, v114, v118
	s_barrier
; #define LAS __attribute__((address_space(3)))
; DI int tr_base(int rlane, int cch, int q, int p) { return img_off(rlane + q, cch + (p >> 1)) + 8 * (p & 1); }
; DI void mlstm_m3_unit(Frame& F, int u) {
;     ...
;     qn += __shfl_xor(qn, 32);
;     __syncthreads();
; #pragma unroll
;     for (int it = 0; it < 4; ++it) { const int idx = tid_ + NTHR * it, row = idx >> 4, ch = idx & 15; *(LAS u32x4*)(imgK + img_off(row, ch)) = kreg[it]; }
;     __syncthreads();
;     u32x4 moreg[8];
;     { const bf16* mop = PROJ + (size_t)(tok0 + tl) * NPROJ + COL_MO + hd * 256 + 128 * dh + 8 * h;
; #pragma unroll
;       for (int nb = 0; nb < 4; ++nb)
; #pragma unroll
;           for (int j2 = 0; j2 < 2; ++j2) moreg[2 * nb + j2] = *(const u32x4*)(mop + 32 * nb + 16 * j2); }
;     float den = 0.f;
;     int vB0[4], vB1[4];
; #pragma unroll
;     for (int nb = 0; nb < 4; ++nb) { vB0[nb] = tr_base(4 * h, 4 * nb + 2 * (g & 1), q4, p4); vB1[nb] = tr_base(8 + 4 * h, 4 * nb + 2 * (g & 1), q4, p4); }
;     const int kmask = ((r & 3) << 2) | ((r >> 2) & 3);
	ds_write_b128 v114, v[74:77]
	v_lshlrev_b32_e32 v75, 2, v115
	v_and_b32_e32 v75, 12, v75
	v_bfe_u32 v76, v115, 2, 2
	v_bitop3_b32 v75, v75, v1, v76 bitop3:0x36
	v_lshlrev_b32_e32 v74, 8, v115
	v_lshlrev_b32_e32 v75, 4, v75
	v_add3_u32 v74, s55, v75, v74
	ds_write_b128 v74, v[66:69]
	v_lshlrev_b32_e32 v67, 2, v116
	v_and_b32_e32 v67, 12, v67
	v_bfe_u32 v68, v116, 2, 2
	v_bitop3_b32 v67, v67, v1, v68 bitop3:0x36
	v_lshlrev_b32_e32 v66, 8, v116
	v_lshlrev_b32_e32 v67, 4, v67
	v_add3_u32 v66, s55, v67, v66
	v_lshlrev_b32_e32 v67, 2, v117
	v_and_b32_e32 v67, 12, v67
	v_bfe_u32 v68, v117, 2, 2
	v_bitop3_b32 v1, v67, v1, v68 bitop3:0x36
	ds_write_b128 v66, v[78:81]
	v_lshlrev_b32_e32 v66, 8, v117
	v_lshlrev_b32_e32 v1, 4, v1
	v_add3_u32 v1, s55, v1, v66
	v_mov_b64_e32 v[66:67], s[14:15]
	v_mad_i64_i32 v[66:67], s[2:3], v170, s74, v[66:67]
	s_lshl_b32 s4, s18, 1
	s_mov_b32 s5, s19
	v_lshl_add_u64 v[66:67], v[66:67], 0, s[4:5]
	s_mov_b32 s29, s19
	v_lshl_add_u64 v[66:67], v[66:67], 0, s[28:29]
	v_lshl_add_u64 v[66:67], v[168:169], 1, v[66:67]
	s_movk_i32 s2, 0x2000
	v_lshl_add_u64 v[68:69], v[66:67], 0, s[30:31]
	v_add_co_u32_e32 v66, vcc, s2, v66
	ds_write_b128 v1, v[70:73]
	s_waitcnt lgkmcnt(0)
	s_barrier
	v_addc_co_u32_e32 v67, vcc, 0, v67, vcc
	global_load_dwordx4 v[138:141], v[68:69], off offset:32 nt
	global_load_dwordx4 v[134:137], v[68:69], off offset:64 nt
	global_load_dwordx4 v[130:133], v[68:69], off offset:96 nt
	global_load_dwordx4 v[126:129], v[68:69], off offset:128 nt
	global_load_dwordx4 v[122:125], v[68:69], off offset:160 nt
	global_load_dwordx4 v[118:121], v[68:69], off offset:192 nt
	global_load_dwordx4 v[142:145], v[66:67], off offset:2048 nt
	global_load_dwordx4 v[114:117], v[68:69], off offset:224 nt
	v_lshlrev_b32_e32 v146, 2, v157
	v_lshlrev_b32_e32 v1, 2, v160
	v_bfe_u32 v66, v166, 5, 2
	v_add_u32_e32 v67, 8, v146
	v_and_b32_e32 v68, 12, v166
	v_bfe_u32 v67, v67, 2, 2
	v_bitop3_b32 v69, v1, v147, v66 bitop3:0x36
	v_bitop3_b32 v71, v1, v148, v66 bitop3:0x36
	v_bitop3_b32 v73, v1, v149, v66 bitop3:0x36
	v_bitop3_b32 v1, v1, v150, v66 bitop3:0x36
	v_lshlrev_b32_e32 v66, 4, v1
	v_bitop3_b32 v1, v68, v150, v67 bitop3:0x36
	v_bitop3_b32 v70, v68, v147, v67 bitop3:0x36
	v_bitop3_b32 v72, v68, v148, v67 bitop3:0x36
	v_bitop3_b32 v74, v68, v149, v67 bitop3:0x36
	v_lshlrev_b32_e32 v67, 4, v1
	v_lshlrev_b32_e32 v1, 2, v166
	v_and_b32_e32 v1, 12, v1
	v_add_u32_e32 v75, 2, v157
	v_add_u32_e32 v76, 4, v157
	v_add_u32_e32 v77, 6, v157
	v_add_u32_e32 v78, 8, v157
	v_add_u32_e32 v79, 10, v157
	v_add_u32_e32 v80, 12, v157
	v_add_u32_e32 v81, 14, v157
	v_bitop3_b32 v68, v1, v157, v160 bitop3:0x36
	v_bitop3_b32 v75, v1, v75, v160 bitop3:0x36
	v_bitop3_b32 v76, v1, v76, v160 bitop3:0x36
	v_bitop3_b32 v77, v1, v77, v160 bitop3:0x36
	v_bitop3_b32 v78, v1, v78, v160 bitop3:0x36
	v_bitop3_b32 v79, v1, v79, v160 bitop3:0x36
	v_bitop3_b32 v80, v1, v80, v160 bitop3:0x36
	v_bitop3_b32 v1, v1, v81, v160 bitop3:0x36
	v_lshlrev_b32_e32 v160, 8, v160
	v_lshl_or_b32 v184, v157, 10, v160
	v_lshlrev_b32_e32 v74, 4, v74
	v_or3_b32 v66, v184, v66, v177
	v_lshlrev_b32_e32 v73, 4, v73
	v_add_u32_e32 v161, s65, v66
	v_or3_b32 v66, v184, v74, v177
	v_lshlrev_b32_e32 v72, 4, v72
	v_add_u32_e32 v179, s65, v66
	v_or3_b32 v66, v184, v73, v177
	v_lshlrev_b32_e32 v71, 4, v71
	v_add_u32_e32 v180, s65, v66
	v_or3_b32 v66, v184, v72, v177
	ds_bpermute_b32 v178, v213, v176
	v_lshlrev_b32_e32 v70, 4, v70
	v_add_u32_e32 v181, s65, v66
	v_or3_b32 v66, v184, v71, v177
	v_lshlrev_b32_e32 v69, 4, v69
	v_add_u32_e32 v182, s65, v66
	v_or3_b32 v66, v184, v70, v177
	v_add_u32_e32 v183, s65, v66
	v_or3_b32 v66, v184, v69, v177
	v_lshlrev_b32_e32 v68, 4, v68
	v_lshlrev_b32_e32 v75, 4, v75
	v_lshlrev_b32_e32 v76, 4, v76
	v_lshlrev_b32_e32 v77, 4, v77
	v_lshlrev_b32_e32 v78, 4, v78
	v_lshlrev_b32_e32 v79, 4, v79
	v_lshlrev_b32_e32 v80, 4, v80
	v_lshlrev_b32_e32 v81, 4, v1
	v_or3_b32 v67, v184, v67, v177
	v_add_u32_e32 v184, s65, v66
	v_lshlrev_b32_e32 v66, 8, v158
	v_add_u32_e32 v1, -8, v172
	v_add_u32_e32 v147, -10, v172
	v_add_u32_e32 v148, -9, v172
	v_add_u32_e32 v149, -16, v172
	v_add_u32_e32 v150, -11, v172
	v_subrev_u32_e32 v151, 18, v172
	v_subrev_u32_e32 v152, 17, v172
	v_subrev_u32_e32 v153, 24, v172
	v_subrev_u32_e32 v154, 19, v172
	v_subrev_u32_e32 v155, 26, v172
	v_subrev_u32_e32 v156, 25, v172
	v_subrev_u32_e32 v159, 27, v172
	v_add_u32_e32 v160, s65, v67
	v_add3_u32 v158, v66, v81, s55
	v_add3_u32 v185, v66, v80, s55
	v_add3_u32 v186, v66, v79, s55
	v_add3_u32 v187, v66, v78, s55
	v_add3_u32 v188, v66, v77, s55
	v_add3_u32 v189, v66, v76, s55
	v_add3_u32 v190, v66, v75, s55
	v_add3_u32 v191, v66, v68, s55
	v_lshl_add_u32 v157, v157, 4, s1
	v_mov_b32_e32 v177, 0
	v_mov_b32_e32 v192, v146

; DI int tr_base(int rlane, int cch, int q, int p) { return img_off(rlane + q, cch + (p >> 1)) + 8 * (p & 1); }
; #define ATT_DECODE(k_, b_, hd_, res_, ib_) do { const int u_ = F.vcu + (k_) * F.G; const int bh_ = u_ >> 4, uu_ = u_ & 15; b_ = bh_ >> 3; hd_ = bh_ & 7; res_ = uu_ / BPR; ib_ = (uu_ % BPR) * 1024; } while (0)
; template <int DIL, bool FIRST, bool LAST>
; DI void attn_phase(Frame& F) {
;     ...
;     const int lane = F.lane, r = lane & 31, h = lane >> 5, g = lane >> 4, i16 = lane & 15, q4 = i16 >> 2, p4 = i16 & 3;
;     const int prow = 4 * F.wave + g, pch = i16 ^ ((g << 2) | (F.wave & 3));
;     const unsigned pdst = (unsigned)F.wave * 1024u;
;     int vB0[4], vB1[4];
; #pragma unroll
;     for (int db = 0; db < 4; ++db) { vB0[db] = tr_base(4 * h, 4 * db + 2 * (g & 1), q4, p4); vB1[db] = tr_base(8 + 4 * h, 4 * db + 2 * (g & 1), q4, p4); }
;     const int kmask = ((r & 3) << 2) | ((r >> 2) & 3);
;     __syncthreads();
;     const int nun = (F.vcu < 256) ? (255 - F.vcu) / F.G + 1 : 0;
;     if (nun > 0) {
;     ...
;         int iu = 0, ij = 0, is = 0, ib_i; const bf16* kv_i;
;         { int b_, hd_, res_; ATT_DECODE(0, b_, hd_, res_, ib_i); kv_i = HMq + HM_PLANE + ((size_t)(b_ * 8 + hd_) * SEQ + res_) * 128; }
;     ...
;         u32x4 qfr[8], on[8]; u32x2 mlx; mlx.x = 0u; mlx.y = 0u;
;     ...
;         ATT_PREFETCH(0, F.wave);
; #pragma unroll
;         for (int jt = 0; jt < PRE; ++jt) ATT_ISSUE1();
.LBB0_690:
	s_cmp_lt_i32 s70, 1
	s_cbranch_scc1 .LBB0_720
	s_add_u32 s0, s94, 0x64000000
	s_addc_u32 s1, s95, 0
	v_lshrrev_b32_e32 v2, 4, v224
	v_lshrrev_b32_e32 v10, 5, v224
	v_and_b32_e32 v1, 15, v0
	v_lshlrev_b32_e32 v3, 2, v2
	s_add_u32 s10, s94, 0x6c000000
	v_bitop3_b32 v3, s25, v1, v3 bitop3:0x36
	v_lshlrev_b32_e32 v12, 2, v10
	v_lshrrev_b32_e32 v1, 3, v224
	s_addc_u32 s11, s95, 0
	v_bfe_u32 v11, v0, 2, 2
	v_and_b32_e32 v1, 2, v1
	v_bfe_u32 v5, v0, 1, 1
	v_and_b32_e32 v7, 12, v0
	v_lshlrev_b32_e32 v9, 3, v0
	v_or_b32_e32 v13, 8, v12
	s_add_u32 s2, s94, 0xa7400000
	v_readlane_b32 s68, v254, 23
	v_or_b32_e32 v4, v12, v11
	v_or_b32_e32 v6, v1, v5
	v_or_b32_e32 v8, v10, v7
	v_and_b32_e32 v9, 8, v9
	v_or_b32_e32 v14, v13, v11
	v_lshrrev_b32_e32 v15, 2, v13
	s_addc_u32 s3, s95, 0
	s_lshl_b32 s8, s68, 10
	s_bfe_u32 s4, s85, 0x30004
	v_lshl_or_b32 v4, v4, 8, v9
	v_lshl_or_b32 v9, v14, 8, v9
	v_bitop3_b32 v1, v1, v8, v5 bitop3:0x36
	v_bitop3_b32 v5, v15, v6, v7 bitop3:0x36
	s_add_u32 s9, s94, 0xab400000
	v_or_b32_e32 v16, v15, v7
	v_lshl_add_u32 v200, v5, 4, v9
	v_bitop3_b32 v5, v6, v8, 4 bitop3:0x36
	s_addc_u32 s12, s95, 0
	s_ashr_i32 s5, s85, 4
	v_lshl_or_b32 v201, v5, 4, v4
	v_bitop3_b32 v5, v6, v16, 4 bitop3:0x36
	s_and_b32 s5, s5, -8
	v_lshl_add_u32 v202, v5, 4, v9
	v_bitop3_b32 v5, v6, v8, 8 bitop3:0x36
	s_or_b32 s4, s5, s4
	v_lshl_or_b32 v203, v5, 4, v4
	v_bitop3_b32 v5, v6, v16, 8 bitop3:0x36
	s_ashr_i32 s5, s4, 31
	v_lshl_add_u32 v204, v5, 4, v9
	v_bitop3_b32 v5, v6, v8, 12 bitop3:0x36
	v_and_b32_e32 v207, 31, v0
	s_lshl_b64 s[6:7], s[4:5], 22
	v_lshl_or_b32 v1, v1, 4, v4
	v_lshl_or_b32 v205, v5, 4, v4
	v_bitop3_b32 v4, v6, v16, 12 bitop3:0x36
	s_add_u32 s6, s9, s6
	v_lshl_or_b32 v178, s68, 5, v207
	v_mov_b32_e32 v179, 0
	v_lshl_add_u32 v206, v4, 4, v9
	v_lshlrev_b32_e32 v4, 2, v0
	s_addc_u32 s7, s12, s7
	s_lshl_b64 s[4:5], s[4:5], 14
	v_lshlrev_b64 v[180:181], 4, v[178:179]
	v_and_b32_e32 v14, 12, v4
	v_lshl_add_u64 v[4:5], s[4:5], 0, v[180:181]
	v_and_or_b32 v4, s85, 15, v4
	v_lshlrev_b64 v[6:7], 8, v[4:5]
	v_lshl_add_u64 v[8:9], s[2:3], 0, v[6:7]
	v_lshlrev_b32_e32 v178, 4, v10
	v_lshl_add_u64 v[8:9], v[8:9], 0, v[178:179]
	s_waitcnt vmcnt(8)
	global_load_dwordx4 v[82:85], v[8:9], off offset:0 nt
	s_waitcnt vmcnt(7)
	global_load_dwordx4 v[86:89], v[8:9], off offset:32 nt
	global_load_dwordx4 v[90:93], v[8:9], off offset:64 nt
	global_load_dwordx4 v[94:97], v[8:9], off offset:0x60 nt
	global_load_dwordx4 v[98:101], v[8:9], off offset:0x80 nt
	global_load_dwordx4 v[102:105], v[8:9], off offset:0xa0 nt
	global_load_dwordx4 v[106:109], v[8:9], off offset:0xc0 nt
	global_load_dwordx4 v[110:113], v[8:9], off offset:0xe0 nt
	v_lshl_add_u64 v[6:7], s[0:1], 0, v[6:7]
	v_lshl_add_u64 v[6:7], v[6:7], 0, v[178:179]
	global_load_dwordx4 v[114:117], v[6:7], off offset:0 nt
	global_load_dwordx4 v[118:121], v[6:7], off offset:32 nt
	global_load_dwordx4 v[122:125], v[6:7], off offset:64 nt
	global_load_dwordx4 v[126:129], v[6:7], off offset:0x60 nt
	global_load_dwordx4 v[130:133], v[6:7], off offset:0x80 nt
	v_or_b32_e32 v2, s23, v2
	global_load_dwordx4 v[134:137], v[6:7], off offset:0xa0 nt
	s_lshl_b32 s4, s85, 8
	global_load_dwordx4 v[138:141], v[6:7], off offset:0xc0 nt
	s_and_b32 s4, s4, 0xf00
	v_add_u32_e32 v208, 0xffffff80, v2
	global_load_dwordx4 v[142:145], v[6:7], off offset:0xe0 nt
	s_add_u32 s78, s6, s4
	v_max_i32_e32 v6, 0, v208
	v_mov_b32_e32 v7, v179
	s_addc_u32 s79, s7, 0
	v_lshlrev_b64 v[6:7], 12, v[6:7]
	v_writelane_b32 v254, s9, 51
	v_lshl_add_u64 v[6:7], s[78:79], 0, v[6:7]
	v_lshlrev_b32_e32 v8, 4, v3
	v_mov_b32_e32 v9, v179
	v_writelane_b32 v254, s10, 52
	v_lshl_add_u64 v[6:7], v[6:7], 0, v[8:9]
	s_mov_b64 s[80:81], 0x4000000
	v_lshl_add_u64 v[4:5], v[4:5], 3, s[10:11]
	global_load_dwordx2 v[182:183], v[4:5], off nt
	v_lshlrev_b32_e32 v4, 3, v3
	s_add_i32 s73, s8, 0
	s_mov_b32 m0, s73
	global_load_lds_dwordx4 v[6:7], off nt
	v_lshl_add_u64 v[6:7], v[6:7], 0, s[80:81]
	v_max_i32_e32 v3, 0x60, v2
	s_add_i32 s4, s73, 0x2000
	s_mov_b32 m0, s4
	global_load_lds_dwordx4 v[6:7], off nt
	v_add_u32_e32 v6, 0xffffffa0, v3
	v_mov_b32_e32 v7, v179
	v_lshlrev_b64 v[6:7], 12, v[6:7]
	v_lshl_add_u64 v[6:7], s[78:79], 0, v[6:7]
	v_lshl_add_u64 v[6:7], v[6:7], 0, v[8:9]
	s_add_i32 s4, s73, 0x4000
	s_mov_b32 m0, s4
	global_load_lds_dwordx4 v[6:7], off nt
	v_lshl_add_u64 v[6:7], v[6:7], 0, s[80:81]
	v_max_i32_e32 v3, 64, v2
	s_addk_i32 s4, 0x2000
	s_mov_b32 m0, s4
	global_load_lds_dwordx4 v[6:7], off nt
	v_subrev_u32_e32 v6, 64, v3
	v_mov_b32_e32 v7, v179
	v_lshlrev_b64 v[6:7], 12, v[6:7]
	v_lshl_add_u64 v[6:7], s[78:79], 0, v[6:7]
	v_lshl_add_u64 v[6:7], v[6:7], 0, v[8:9]
; #define LAS __attribute__((address_space(3)))
; DI f32x16 mfma32(bf16x8 a, bf16x8 b, f32x16 c) { return __builtin_amdgcn_mfma_f32_32x32x16_bf16(a, b, c, 0, 0, 0); }
; DI int crow(int reg, int h) { return (reg & 3) + 8 * (reg >> 2) + 4 * h; }
; DI bf16x8 tr_frag2(const LAS unsigned char* img, int ba, int bb, int off) { const s16x4 lo = tr16(img + ba + off), hi = tr16(img + bb + off); return __builtin_shufflevector(lo, hi, 0, 1, 2, 3, 4, 5, 6, 7); }
; template <int DIL, bool FIRST, bool LAST>
; DI void attn_phase(Frame& F) {
;     ...
;         u32x4 qfr[8], on[8]; u32x2 mlx; mlx.x = 0u; mlx.y = 0u;
;     ...
;         ATT_PREFETCH(0, F.wave);
; #pragma unroll
;         for (int jt = 0; jt < PRE; ++jt) ATT_ISSUE1();
;         int cs = 0;
;         f32x16 o[4]; float m = -1e30f, l = 0.f;
;     ...
;                     const LAS unsigned char* krow = kimg + 256 * r;
;                     bf16x8 ka[8];
; #pragma unroll
;                     for (int kk = 0; kk < 8; ++kk) ka[kk] = *(const LAS bf16x8*)(krow + 16 * ((2 * kk + h) ^ kmask));
;                     __builtin_amdgcn_sched_barrier(0);
; #pragma unroll
;                     for (int kk = 0; kk < 8; ++kk) s = mfma32(ka[kk], __builtin_bit_cast(bf16x8, qfr[kk]), s);
;                     bf16x8 va[2][4];
; #pragma unroll
;                     for (int s2 = 0; s2 < 2; ++s2)
; #pragma unroll
;                         for (int db = 0; db < 4; ++db) va[s2][db] = tr_frag2(vi, vB0[db], vB1[db], s2 * 4096);
;                     __builtin_amdgcn_sched_barrier(0);
;                     { const int kb = i0 - 128 + 32 * kt;
;                       if (kt == 0 || kt == 4 || kb < 0) {
; #pragma unroll
;                         for (int e = 0; e < 16; ++e) { const int ce = crow(e, h); const bool bad = ((kb + ce) < 0) || (kt == 0 && ce < r) || (kt == 4 && ce > r); if (bad) s[e] = -1e30f; } } }
	s_add_i32 s4, s73, 0x8000
	s_mov_b32 m0, s4
	global_load_lds_dwordx4 v[6:7], off nt
	v_lshl_add_u64 v[6:7], v[6:7], 0, s[80:81]
	v_max_i32_e32 v3, 32, v2
	s_addk_i32 s4, 0x2000
	s_mov_b32 m0, s4
	global_load_lds_dwordx4 v[6:7], off nt
	v_subrev_u32_e32 v6, 32, v3
	v_mov_b32_e32 v7, v179
	v_lshlrev_b64 v[6:7], 12, v[6:7]
	v_lshl_add_u64 v[6:7], s[78:79], 0, v[6:7]
	v_lshl_add_u64 v[6:7], v[6:7], 0, v[8:9]
	s_add_i32 s4, s73, 0xc000
	s_mov_b32 m0, s4
	global_load_lds_dwordx4 v[6:7], off nt
	v_lshl_add_u64 v[6:7], v[6:7], 0, s[80:81]
	v_mov_b32_e32 v3, v179
	s_addk_i32 s4, 0x2000
	s_mov_b32 m0, s4
	global_load_lds_dwordx4 v[6:7], off nt
	v_lshlrev_b64 v[6:7], 12, v[2:3]
	v_add_u32_e32 v2, 32, v2
	v_lshl_add_u64 v[6:7], s[78:79], 0, v[6:7]
	s_add_i32 s4, s73, 0x10000
	v_lshlrev_b64 v[2:3], 12, v[2:3]
	v_lshl_add_u64 v[6:7], v[6:7], 0, v[8:9]
	s_mov_b32 m0, s4
	global_load_lds_dwordx4 v[6:7], off nt
	s_addk_i32 s4, 0x2000
	v_lshl_add_u64 v[2:3], s[78:79], 0, v[2:3]
	v_lshl_add_u64 v[6:7], v[6:7], 0, s[80:81]
	s_mov_b32 m0, s4
	global_load_lds_dwordx4 v[6:7], off nt
	v_lshl_add_u64 v[2:3], v[2:3], 0, v[8:9]
	s_add_i32 s4, s73, 0x14000
	s_mov_b32 m0, s4
	global_load_lds_dwordx4 v[2:3], off nt
	v_lshl_add_u64 v[2:3], v[2:3], 0, s[80:81]
	s_addk_i32 s4, 0x2000
	s_mov_b32 m0, s4
	global_load_lds_dwordx4 v[2:3], off nt
	v_lshl_add_u64 v[2:3], s[94:95], 0, v[178:179]
	s_mov_b64 s[4:5], 0x6c400000
	v_or_b32_e32 v15, v14, v11
	v_lshl_add_u64 v[184:185], v[2:3], 0, s[4:5]
	v_bitop3_b32 v2, v14, v10, v11 bitop3:0x36
	v_lshlrev_b32_e32 v211, 4, v2
	v_bitop3_b32 v2, v10, v15, 2 bitop3:0x36
	v_lshlrev_b32_e32 v212, 4, v2
	v_bitop3_b32 v2, v10, v15, 4 bitop3:0x36
	v_lshlrev_b32_e32 v213, 4, v2
	v_bitop3_b32 v2, v10, v15, 6 bitop3:0x36
	v_lshlrev_b32_e32 v214, 4, v2
	v_bitop3_b32 v2, v10, v15, 8 bitop3:0x36
	v_lshlrev_b32_e32 v215, 4, v2
	v_bitop3_b32 v2, v10, v15, 10 bitop3:0x36
	v_lshlrev_b32_e32 v216, 4, v2
	v_bitop3_b32 v2, v10, v15, 12 bitop3:0x36
	v_lshlrev_b32_e32 v217, 4, v2
	v_bitop3_b32 v2, v10, v15, 14 bitop3:0x36
	v_lshlrev_b32_e32 v218, 4, v2
	v_or_b32_e32 v2, 1, v12
	v_cmp_lt_u32_e64 s[6:7], v2, v207
	v_or_b32_e32 v2, 2, v12
	s_mov_b32 s72, s12
	v_writelane_b32 v254, s11, 53
	v_cmp_lt_u32_e64 s[10:11], v2, v207
	v_cmp_gt_u32_e64 s[12:13], v2, v207
	v_or_b32_e32 v2, 3, v12
	v_cmp_lt_u32_e64 s[14:15], v2, v207
	v_cmp_gt_u32_e64 s[16:17], v2, v207
	v_or_b32_e32 v2, 9, v12
	v_cmp_lt_u32_e64 s[22:23], v2, v207
	v_cmp_gt_u32_e64 s[24:25], v2, v207
	v_or_b32_e32 v2, 10, v12
	v_cmp_lt_u32_e64 s[26:27], v2, v207
	v_cmp_gt_u32_e64 s[28:29], v2, v207
	v_or_b32_e32 v2, 11, v12
	v_cmp_lt_u32_e64 s[30:31], v2, v207
	v_cmp_gt_u32_e64 s[34:35], v2, v207
	v_or_b32_e32 v2, 16, v12
	v_cmp_lt_u32_e64 s[36:37], v2, v207
	v_cmp_gt_u32_e64 s[38:39], v2, v207
	v_or_b32_e32 v2, 17, v12
	v_cmp_lt_u32_e64 s[40:41], v2, v207
	v_cmp_gt_u32_e64 s[42:43], v2, v207
	v_or_b32_e32 v2, 18, v12
	v_cmp_lt_u32_e64 s[44:45], v2, v207
	v_cmp_gt_u32_e64 s[46:47], v2, v207
	v_or_b32_e32 v2, 19, v12
	v_cmp_lt_u32_e64 s[48:49], v2, v207
	v_cmp_gt_u32_e64 s[50:51], v2, v207
	v_or_b32_e32 v2, 24, v12
	v_cmp_lt_u32_e64 s[52:53], v2, v207
	v_cmp_gt_u32_e64 s[54:55], v2, v207
	v_or_b32_e32 v2, 25, v12
	v_cmp_lt_u32_e64 s[56:57], v2, v207
	v_cmp_gt_u32_e64 s[58:59], v2, v207
	v_or_b32_e32 v2, 26, v12
	v_cmp_lt_u32_e64 s[60:61], v2, v207
	v_cmp_gt_u32_e64 s[62:63], v2, v207
	v_or_b32_e32 v2, 27, v12
	v_writelane_b32 v255, s88, 0
	v_cmp_lt_u32_e64 s[64:65], v2, v207
	v_cmp_gt_u32_e64 s[66:67], v2, v207
	v_mbcnt_lo_u32_b32 v2, -1, 0
	v_writelane_b32 v255, s89, 1
	s_mov_b32 s77, 0
	v_lshl_add_u64 v[186:187], s[2:3], 0, v[178:179]
	v_lshl_add_u64 v[188:189], s[0:1], 0, v[178:179]
	v_or_b32_e32 v209, 0x100, v207
	v_lshlrev_b32_e32 v210, 8, v207
	s_mov_b32 s33, 6
	v_sub_u32_e32 v219, 0, v12
	v_cmp_lt_u32_e64 s[2:3], v12, v207
	v_cmp_gt_u32_e64 s[4:5], v12, v207
	v_cmp_ge_u32_e64 s[8:9], v12, v207
	v_sub_u32_e32 v220, -8, v12
	v_cmp_lt_u32_e64 s[18:19], v13, v207
	v_cmp_gt_u32_e64 s[20:21], v13, v207
	v_xor_b32_e32 v221, -9, v12
	v_xor_b32_e32 v222, -10, v12
	v_xor_b32_e32 v223, -11, v12
	v_sub_u32_e32 v225, -16, v12
	v_xor_b32_e32 v226, 0xffffffef, v12
	v_xor_b32_e32 v227, 0xffffffee, v12
	v_xor_b32_e32 v228, 0xffffffed, v12
	v_sub_u32_e32 v229, 0xffffffe8, v12
	v_xor_b32_e32 v230, 0xffffffe7, v12
	v_xor_b32_e32 v231, 0xffffffe6, v12
	v_xor_b32_e32 v232, 0xffffffe5, v12
	s_sub_i32 s96, 0, s68
	v_mov_b32_e32 v233, 0xf149f2ca
	v_lshlrev_b32_e32 v190, 1, v4
	v_mbcnt_hi_u32_b32 v234, -1, v2
	s_mov_b32 s75, 0
	s_mov_b32 s74, 6
	s_mov_b32 s82, 0
	v_mov_b32_e32 v236, 0xf149f2ca
	v_mov_b32_e32 v235, 0
	s_mov_b32 s83, 0
	s_waitcnt vmcnt(0)
	s_branch .LBB0_693

.LBB0_695:
	v_lshl_add_u32 v66, s33, 5, v208
	v_max_i32_e32 v178, 0, v66
	v_lshlrev_b64 v[66:67], 12, v[178:179]
	v_lshl_add_u64 v[66:67], s[78:79], 0, v[66:67]
	v_mov_b32_e32 v191, v179
	s_and_b32 s0, s76, 0x1c000
	v_lshl_add_u64 v[66:67], v[66:67], 0, v[190:191]
	s_add_i32 s0, s73, s0
	s_mov_b32 m0, s0
	global_load_lds_dwordx4 v[66:67], off nt
	v_lshl_add_u64 v[66:67], v[66:67], 0, s[80:81]
	s_addk_i32 s0, 0x2000
	s_mov_b32 m0, s0
	global_load_lds_dwordx4 v[66:67], off nt
	s_add_i32 s33, s33, 1
	s_cmp_lg_u32 s33, 36
	s_cbranch_scc1 .LBB0_698
	s_add_i32 s0, s75, 1
	s_cmp_ge_i32 s0, s70
	s_mov_b32 s33, 35
	s_cbranch_scc1 .LBB0_698
	v_readlane_b32 s1, v254, 2
	s_mul_i32 s1, s0, s1
	v_readlane_b32 s33, v254, 43
	s_add_i32 s1, s1, s33
	s_ashr_i32 s68, s1, 4
	s_bfe_u32 s33, s1, 0x30004
	s_and_b32 s68, s68, -8
	s_or_b32 s68, s68, s33
	s_ashr_i32 s69, s68, 31
	s_lshl_b64 s[68:69], s[68:69], 22
	v_readlane_b32 s33, v254, 51
	s_add_u32 s33, s33, s68
	s_addc_u32 s68, s72, s69
	s_lshl_b32 s1, s1, 8
	s_and_b32 s1, s1, 0xf00
	s_add_u32 s78, s33, s1
	s_addc_u32 s79, s68, 0
	s_mov_b32 s33, 0
	s_mov_b32 s75, s0

; DI unsigned cvtpk(float lo, float hi) { f32x2 v = {lo, hi}; bf16x2_t b = __builtin_convertvector(v, bf16x2_t); return __builtin_bit_cast(unsigned, b); }
; DI f32x16 mfma32(bf16x8 a, bf16x8 b, f32x16 c) { return __builtin_amdgcn_mfma_f32_32x32x16_bf16(a, b, c, 0, 0, 0); }
; template <int DIL, bool FIRST, bool LAST>
; DI void attn_phase(Frame& F) {
;     ...
;                     float rs = 0.f;
; #pragma unroll
;                     for (int e = 0; e < 16; ++e) { s[e] = __builtin_amdgcn_exp2f(s[e] - m); rs += s[e]; }
;                     rs += __shfl_xor(rs, 32); l += rs;
;                     bf16x8 pb[2];
; #pragma unroll
;                     for (int s2 = 0; s2 < 2; ++s2) { u32x4 w; w.x = cvtpk(s[8 * s2], s[8 * s2 + 1]); w.y = cvtpk(s[8 * s2 + 2], s[8 * s2 + 3]); w.z = cvtpk(s[8 * s2 + 4], s[8 * s2 + 5]); w.w = cvtpk(s[8 * s2 + 6], s[8 * s2 + 7]);
;                         pb[s2] = __builtin_bit_cast(bf16x8, w); }
; #pragma unroll
;                     for (int s2 = 0; s2 < 2; ++s2) {
; #pragma unroll
;                         for (int db = 0; db < 4; ++db) o[db] = mfma32(va[s2][db], pb[s2], o[db]);
;                     }
.LBB0_712:
	v_sub_f32_e32 v66, v66, v236
	v_exp_f32_e32 v66, v66
	v_sub_f32_e32 v67, v67, v236
	v_exp_f32_e32 v67, v67
	v_sub_f32_e32 v68, v68, v236
	v_exp_f32_e32 v68, v68
	v_sub_f32_e32 v69, v69, v236
	v_exp_f32_e32 v69, v69
	v_sub_f32_e32 v70, v70, v236
	v_add_f32_e32 v191, 0, v66
	v_exp_f32_e32 v70, v70
	v_sub_f32_e32 v71, v71, v236
	v_add_f32_e32 v191, v67, v191
	v_exp_f32_e32 v71, v71
	v_sub_f32_e32 v72, v72, v236
	v_sub_f32_e32 v73, v73, v236
	v_add_f32_e32 v191, v68, v191
	v_exp_f32_e32 v72, v72
	v_exp_f32_e32 v73, v73
	v_add_f32_e32 v191, v69, v191
	v_sub_f32_e32 v74, v74, v236
	v_add_f32_e32 v191, v70, v191
	v_exp_f32_e32 v74, v74
	v_sub_f32_e32 v75, v75, v236
	v_add_f32_e32 v191, v71, v191
	v_exp_f32_e32 v75, v75
	v_sub_f32_e32 v76, v76, v236
	v_add_f32_e32 v191, v72, v191
	v_exp_f32_e32 v76, v76
	v_sub_f32_e32 v77, v77, v236
	v_cvt_pk_bf16_f32 v66, v66, v67
	v_cvt_pk_bf16_f32 v67, v68, v69
	v_cvt_pk_bf16_f32 v68, v70, v71
	v_cvt_pk_bf16_f32 v69, v72, v73
	v_add_f32_e32 v191, v73, v191
	v_exp_f32_e32 v77, v77
	v_sub_f32_e32 v78, v78, v236
	v_mfma_f32_32x32x16_bf16 v[2:17], v[170:173], v[66:69], v[2:17]
	v_add_f32_e32 v191, v74, v191
	v_exp_f32_e32 v78, v78
	v_sub_f32_e32 v79, v79, v236
	v_add_f32_e32 v191, v75, v191
	v_exp_f32_e32 v79, v79
	v_sub_f32_e32 v80, v80, v236
	v_sub_f32_e32 v81, v81, v236
	v_mfma_f32_32x32x16_bf16 v[18:33], v[174:177], v[66:69], v[18:33]
	v_add_f32_e32 v191, v76, v191
	v_exp_f32_e32 v80, v80
	v_exp_f32_e32 v81, v81
	v_add_f32_e32 v191, v77, v191
	v_add_f32_e32 v191, v78, v191
	v_add_f32_e32 v191, v79, v191
	v_add_f32_e32 v191, v80, v191
	v_mfma_f32_32x32x16_bf16 v[34:49], v[166:169], v[66:69], v[34:49]
	v_cvt_pk_bf16_f32 v70, v74, v75
	v_cvt_pk_bf16_f32 v71, v76, v77
	v_cvt_pk_bf16_f32 v72, v78, v79
	v_cvt_pk_bf16_f32 v73, v80, v81
	v_add_f32_e32 v191, v81, v191
	ds_bpermute_b32 v178, v178, v191
	s_andn2_b64 vcc, exec, s[86:87]
	v_mfma_f32_32x32x16_bf16 v[50:65], v[162:165], v[66:69], v[50:65]
	s_waitcnt lgkmcnt(0)
	v_add_f32_e32 v178, v191, v178
	v_add_f32_e32 v235, v235, v178
	v_mfma_f32_32x32x16_bf16 v[2:17], v[158:161], v[70:73], v[2:17]
	v_mfma_f32_32x32x16_bf16 v[18:33], v[154:157], v[70:73], v[18:33]
	v_mfma_f32_32x32x16_bf16 v[34:49], v[150:153], v[70:73], v[34:49]
	v_mfma_f32_32x32x16_bf16 v[50:65], v[146:149], v[70:73], v[50:65]
	s_cbranch_vccnz .LBB0_694
; DI unsigned cvtpk(float lo, float hi) { f32x2 v = {lo, hi}; bf16x2_t b = __builtin_convertvector(v, bf16x2_t); return __builtin_bit_cast(unsigned, b); }
; template <int DIL, bool FIRST, bool LAST>
; DI void attn_phase(Frame& F) {
;     ...
;                     if (kt == 4) {
;                         const size_t hrow = (size_t)(b * 8 + hd) * SEQ + (size_t)(i0 + r) * DIL + res;
;                         if (LAST) {
;                             const size_t rowq = (size_t)b * SEQ + (size_t)(i0 + r) * DIL + res;
;                             const float il = 1.0f / l;
;                             bf16* mp = MIX + rowq * DM + hd * 128 + 8 * h;
; #pragma unroll
;                             for (int db = 0; db < 4; ++db)
; #pragma unroll
;                                 for (int j2 = 0; j2 < 2; ++j2) { u32x2 w2[2];
; #pragma unroll
;                                     for (int q2 = 0; q2 < 2; ++q2) { const int g4 = 2 * j2 + q2; w2[q2].x = cvtpk(o[db][4 * g4] * il, o[db][4 * g4 + 1] * il); w2[q2].y = cvtpk(o[db][4 * g4 + 2] * il, o[db][4 * g4 + 3] * il); }
;                                     swap32(w2[0], w2[1]); u32x4 w; w.x = w2[0].x; w.y = w2[0].y; w.z = w2[1].x; w.w = w2[1].y;
;                                     *(u32x4*)(mp + 32 * db + 16 * j2) = w; }
;                         } else {
;                             bf16* ostp = OST + hrow * 128 + 8 * h; float* mlp = ML + hrow * 2;
; #pragma unroll
;                             for (int db = 0; db < 4; ++db)
; #pragma unroll
;                                 for (int j2 = 0; j2 < 2; ++j2) { u32x2 w2[2];
; #pragma unroll
;                                     for (int q2 = 0; q2 < 2; ++q2) { const int g4 = 2 * j2 + q2; w2[q2].x = cvtpk(o[db][4 * g4], o[db][4 * g4 + 1]); w2[q2].y = cvtpk(o[db][4 * g4 + 2], o[db][4 * g4 + 3]); }
;                                     swap32(w2[0], w2[1]); u32x4 w; w.x = w2[0].x; w.y = w2[0].y; w.z = w2[1].x; w.w = w2[1].y;
;                                     *(u32x4*)(ostp + 32 * db + 16 * j2) = w; }
;                             if (h == 0) { f32x2 mlv; mlv[0] = m; mlv[1] = l; *(f32x2*)mlp = mlv; }
;                         }
;                         if (mq < 3) ATT_PREFETCH(k, qt + 8); else if (k + 1 < nun) ATT_PREFETCH(k + 1, F.wave);
	v_div_scale_f32 v68, s[0:1], v235, v235, 1.0
	v_rcp_f32_e32 v69, v68
	v_or_b32_e32 v66, s97, v207
	v_ashrrev_i32_e32 v67, 31, v66
	v_lshlrev_b64 v[66:67], 16, v[66:67]
	v_fma_f32 v70, -v68, v69, 1.0
	v_fmac_f32_e32 v69, v70, v69
	v_div_scale_f32 v70, vcc, 1.0, v235, 1.0
	v_mul_f32_e32 v71, v70, v69
	v_fma_f32 v72, -v68, v71, v70
	v_fmac_f32_e32 v71, v72, v69
	v_fma_f32 v68, -v68, v71, v70
	v_div_fmas_f32 v68, v68, v69, v71
	v_div_fixup_f32 v70, v68, v235, 1.0
	v_lshl_add_u64 v[72:73], v[192:193], 0, v[66:67]
	v_pk_mul_f32 v[66:67], v[2:3], v[70:71] op_sel_hi:[1,0]
	v_pk_mul_f32 v[68:69], v[4:5], v[70:71] op_sel_hi:[1,0]
	v_cvt_pk_bf16_f32 v66, v66, v67
	v_cvt_pk_bf16_f32 v67, v68, v69
	v_pk_mul_f32 v[68:69], v[6:7], v[70:71] op_sel_hi:[1,0]
	v_pk_mul_f32 v[74:75], v[8:9], v[70:71] op_sel_hi:[1,0]
	v_cvt_pk_bf16_f32 v68, v68, v69
	v_cvt_pk_bf16_f32 v69, v74, v75
	s_nop 0
	v_permlane32_swap_b32_e32 v66, v68
	v_permlane32_swap_b32_e32 v67, v69
	global_store_dwordx4 v[72:73], v[66:69], off
	v_pk_mul_f32 v[74:75], v[16:17], v[70:71] op_sel_hi:[1,0]
	s_cmp_gt_i32 s77, 2
	v_pk_mul_f32 v[66:67], v[10:11], v[70:71] op_sel_hi:[1,0]
	v_pk_mul_f32 v[68:69], v[12:13], v[70:71] op_sel_hi:[1,0]
	v_cvt_pk_bf16_f32 v66, v66, v67
	v_cvt_pk_bf16_f32 v67, v68, v69
	v_pk_mul_f32 v[68:69], v[14:15], v[70:71] op_sel_hi:[1,0]
	s_mov_b64 s[0:1], -1
	v_cvt_pk_bf16_f32 v68, v68, v69
	v_cvt_pk_bf16_f32 v69, v74, v75
	s_nop 0
	v_permlane32_swap_b32_e32 v66, v68
	v_permlane32_swap_b32_e32 v67, v69
	global_store_dwordx4 v[72:73], v[66:69], off offset:32
	v_pk_mul_f32 v[74:75], v[24:25], v[70:71] op_sel_hi:[1,0]
	s_nop 0
	v_pk_mul_f32 v[66:67], v[18:19], v[70:71] op_sel_hi:[1,0]
	v_pk_mul_f32 v[68:69], v[20:21], v[70:71] op_sel_hi:[1,0]
	v_cvt_pk_bf16_f32 v66, v66, v67
	v_cvt_pk_bf16_f32 v67, v68, v69
	v_pk_mul_f32 v[68:69], v[22:23], v[70:71] op_sel_hi:[1,0]
	s_nop 0
	v_cvt_pk_bf16_f32 v68, v68, v69
	v_cvt_pk_bf16_f32 v69, v74, v75
	s_nop 0
	v_permlane32_swap_b32_e32 v66, v68
	v_permlane32_swap_b32_e32 v67, v69
	global_store_dwordx4 v[72:73], v[66:69], off offset:64
	v_pk_mul_f32 v[74:75], v[32:33], v[70:71] op_sel_hi:[1,0]
	s_nop 0
	v_pk_mul_f32 v[66:67], v[26:27], v[70:71] op_sel_hi:[1,0]
	v_pk_mul_f32 v[68:69], v[28:29], v[70:71] op_sel_hi:[1,0]
	v_cvt_pk_bf16_f32 v66, v66, v67
	v_cvt_pk_bf16_f32 v67, v68, v69
	v_pk_mul_f32 v[68:69], v[30:31], v[70:71] op_sel_hi:[1,0]
	s_nop 0
	v_cvt_pk_bf16_f32 v68, v68, v69
	v_cvt_pk_bf16_f32 v69, v74, v75
	s_nop 0
	v_permlane32_swap_b32_e32 v66, v68
	v_permlane32_swap_b32_e32 v67, v69
	global_store_dwordx4 v[72:73], v[66:69], off offset:96
	v_pk_mul_f32 v[74:75], v[40:41], v[70:71] op_sel_hi:[1,0]
	s_nop 0
	v_pk_mul_f32 v[66:67], v[34:35], v[70:71] op_sel_hi:[1,0]
	v_pk_mul_f32 v[68:69], v[36:37], v[70:71] op_sel_hi:[1,0]
	v_cvt_pk_bf16_f32 v66, v66, v67
	v_cvt_pk_bf16_f32 v67, v68, v69
	v_pk_mul_f32 v[68:69], v[38:39], v[70:71] op_sel_hi:[1,0]
	s_nop 0
	v_cvt_pk_bf16_f32 v68, v68, v69
	v_cvt_pk_bf16_f32 v69, v74, v75
	s_nop 0
	v_permlane32_swap_b32_e32 v66, v68
	v_permlane32_swap_b32_e32 v67, v69
	global_store_dwordx4 v[72:73], v[66:69], off offset:128
	v_pk_mul_f32 v[74:75], v[48:49], v[70:71] op_sel_hi:[1,0]
	s_nop 0
	v_pk_mul_f32 v[66:67], v[42:43], v[70:71] op_sel_hi:[1,0]
	v_pk_mul_f32 v[68:69], v[44:45], v[70:71] op_sel_hi:[1,0]
	v_cvt_pk_bf16_f32 v66, v66, v67
	v_cvt_pk_bf16_f32 v67, v68, v69
	v_pk_mul_f32 v[68:69], v[46:47], v[70:71] op_sel_hi:[1,0]
	s_nop 0
	v_cvt_pk_bf16_f32 v68, v68, v69
	v_cvt_pk_bf16_f32 v69, v74, v75
	s_nop 0
	v_permlane32_swap_b32_e32 v66, v68
	v_permlane32_swap_b32_e32 v67, v69
	global_store_dwordx4 v[72:73], v[66:69], off offset:160
	v_pk_mul_f32 v[74:75], v[56:57], v[70:71] op_sel_hi:[1,0]
	s_nop 0
	v_pk_mul_f32 v[66:67], v[50:51], v[70:71] op_sel_hi:[1,0]
	v_pk_mul_f32 v[68:69], v[52:53], v[70:71] op_sel_hi:[1,0]
	v_cvt_pk_bf16_f32 v66, v66, v67
	v_cvt_pk_bf16_f32 v67, v68, v69
	v_pk_mul_f32 v[68:69], v[54:55], v[70:71] op_sel_hi:[1,0]
	s_nop 0
	v_cvt_pk_bf16_f32 v68, v68, v69
	v_cvt_pk_bf16_f32 v69, v74, v75
	s_nop 0
	v_permlane32_swap_b32_e32 v66, v68
	v_permlane32_swap_b32_e32 v67, v69
	global_store_dwordx4 v[72:73], v[66:69], off offset:192
	s_nop 1
	v_pk_mul_f32 v[66:67], v[58:59], v[70:71] op_sel_hi:[1,0]
	v_pk_mul_f32 v[68:69], v[60:61], v[70:71] op_sel_hi:[1,0]
	v_cvt_pk_bf16_f32 v66, v66, v67
	v_cvt_pk_bf16_f32 v67, v68, v69
	v_pk_mul_f32 v[68:69], v[62:63], v[70:71] op_sel_hi:[1,0]
	v_pk_mul_f32 v[70:71], v[64:65], v[70:71] op_sel_hi:[1,0]
	v_cvt_pk_bf16_f32 v68, v68, v69
	v_cvt_pk_bf16_f32 v69, v70, v71
	s_nop 0
	v_permlane32_swap_b32_e32 v66, v68
	v_permlane32_swap_b32_e32 v67, v69
	global_store_dwordx4 v[72:73], v[66:69], off offset:224
	s_cbranch_scc0 .LBB0_717
	v_readlane_b32 s0, v254, 54
	v_readlane_b32 s1, v254, 55
	s_andn2_b64 vcc, exec, s[0:1]
	s_cbranch_vccnz .LBB0_716
	global_load_dwordx4 v[82:85], v[194:195], off offset:0 nt
	global_load_dwordx4 v[86:89], v[194:195], off offset:32 nt
	global_load_dwordx4 v[90:93], v[194:195], off offset:64 nt
	global_load_dwordx4 v[94:97], v[194:195], off offset:0x60 nt
	global_load_dwordx4 v[98:101], v[194:195], off offset:0x80 nt
	global_load_dwordx4 v[102:105], v[194:195], off offset:0xa0 nt
	global_load_dwordx4 v[106:109], v[194:195], off offset:0xc0 nt
	global_load_dwordx4 v[110:113], v[194:195], off offset:0xe0 nt
	global_load_dwordx4 v[114:117], v[196:197], off offset:0 nt
	global_load_dwordx4 v[118:121], v[196:197], off offset:32 nt
	global_load_dwordx4 v[122:125], v[196:197], off offset:64 nt
	global_load_dwordx4 v[126:129], v[196:197], off offset:0x60 nt
	global_load_dwordx4 v[130:133], v[196:197], off offset:0x80 nt
	global_load_dwordx4 v[134:137], v[196:197], off offset:0xa0 nt
	global_load_dwordx4 v[138:141], v[196:197], off offset:0xc0 nt
	global_load_dwordx4 v[142:145], v[196:197], off offset:0xe0 nt
	global_load_dwordx2 v[182:183], v[198:199], off nt

; template <int DIL, bool FIRST, bool LAST>
; DI void attn_phase(Frame& F) {
;     ...
;                         if (mq < 3) ATT_PREFETCH(k, qt + 8); else if (k + 1 < nun) ATT_PREFETCH(k + 1, F.wave);
.LBB0_717:
	s_andn2_b64 vcc, exec, s[0:1]
	s_cbranch_vccnz .LBB0_694
	v_add_u32_e32 v66, s97, v209
	v_ashrrev_i32_e32 v67, 31, v66
	v_lshl_add_u64 v[66:67], v[66:67], 4, s[84:85]
	v_lshlrev_b64 v[68:69], 8, v[66:67]
	v_lshl_add_u64 v[70:71], v[186:187], 0, v[68:69]
	global_load_dwordx4 v[82:85], v[70:71], off offset:0 nt
	global_load_dwordx4 v[86:89], v[70:71], off offset:32 nt
	global_load_dwordx4 v[90:93], v[70:71], off offset:64 nt
	global_load_dwordx4 v[94:97], v[70:71], off offset:0x60 nt
	global_load_dwordx4 v[98:101], v[70:71], off offset:0x80 nt
	global_load_dwordx4 v[102:105], v[70:71], off offset:0xa0 nt
	global_load_dwordx4 v[106:109], v[70:71], off offset:0xc0 nt
	global_load_dwordx4 v[110:113], v[70:71], off offset:0xe0 nt
	v_lshl_add_u64 v[68:69], v[188:189], 0, v[68:69]
	global_load_dwordx4 v[114:117], v[68:69], off offset:0 nt
	global_load_dwordx4 v[118:121], v[68:69], off offset:32 nt
	global_load_dwordx4 v[122:125], v[68:69], off offset:64 nt
	global_load_dwordx4 v[126:129], v[68:69], off offset:0x60 nt
	global_load_dwordx4 v[130:133], v[68:69], off offset:0x80 nt
	global_load_dwordx4 v[134:137], v[68:69], off offset:0xa0 nt
	global_load_dwordx4 v[138:141], v[68:69], off offset:0xc0 nt
	v_readlane_b32 s0, v254, 52
	global_load_dwordx4 v[142:145], v[68:69], off offset:0xe0 nt
	v_readlane_b32 s1, v254, 53
	s_nop 1
	v_lshl_add_u64 v[66:67], v[66:67], 3, s[0:1]
	global_load_dwordx2 v[182:183], v[66:67], off nt
	s_branch .LBB0_694
